# v71 + last tile of the gates and out GEMM calls stores write-through (sc1) ahead of the grid barrier's L2 write-back
# speedup vs baseline: 1.0029x; 1.0029x over previous
; __device__ __forceinline__ float fsigmoid(float x) { return __builtin_amdgcn_rcpf(1.0f + __builtin_amdgcn_exp2f(-1.44269504f * x)); }
;     __device__ __forceinline__ void operator()(AccRef acc, const GUnit& u, int wr, int wc, int fr, int fq) const {
;         const int pm = u.x0, pn = u.x1; unsigned char* base = (pn < 8 ? GZF : GZS) + (size_t)(pm * 256 + wr * 64 + fr) * D + (pn & 7) * 256 + wc * 64 + 16 * fq;
; #pragma unroll
;         for (int ai = 0; ai < 2; ++ai)
; #pragma unroll
;             for (int m = 0; m < 4; ++m) { u32x4 w;
; #pragma unroll
;                 for (int bj = 0; bj < 2; ++bj)
; #pragma unroll
;                     for (int n = 0; n < 2; ++n) { const f32x4 v = acc[ai][bj][m][n]; w[bj * 2 + n] = pk4_u8(fsigmoid(v[0] * W8_INV), fsigmoid(v[1] * W8_INV), fsigmoid(v[2] * W8_INV), fsigmoid(v[3] * W8_INV)); }
;                 *(u32x4*)(base + (size_t)(ai * 128 + m * 16) * D) = w; }
.LBB0_431:
	s_cmp_eq_u64 s[0:1], 0
	s_cbranch_scc1 .Lwt_g
	s_nop 15
	s_nop 7
	v_lshl_add_u32 v2, s8, 8, v190
	v_mul_f32_e32 v4, 0xbcb8aa3b, v158
	v_mul_f32_e32 v5, 0xbcb8aa3b, v159
	v_mul_f32_e32 v6, 0xbcb8aa3b, v160
	v_mul_f32_e32 v7, 0xbcb8aa3b, v161
	v_exp_f32_e32 v4, v4
	v_exp_f32_e32 v5, v5
	v_exp_f32_e32 v6, v6
	v_exp_f32_e32 v7, v7
	v_add_f32_e32 v4, 1.0, v4
	v_add_f32_e32 v5, 1.0, v5
	v_add_f32_e32 v6, 1.0, v6
	v_add_f32_e32 v7, 1.0, v7
	v_rcp_f32_e32 v4, v4
	v_rcp_f32_e32 v5, v5
	v_rcp_f32_e32 v6, v6
	v_rcp_f32_e32 v7, v7
	v_fmamk_f32 v4, v4, 0x437f0000, v196
	v_fmamk_f32 v5, v5, 0x437f0000, v196
	v_fmamk_f32 v6, v6, 0x437f0000, v196
	v_fmamk_f32 v7, v7, 0x437f0000, v196
	v_perm_b32 v4, v5, v4, s67
	v_perm_b32 v5, v7, v6, s67
	v_mul_f32_e32 v6, 0xbcb8aa3b, v154
	v_mul_f32_e32 v7, 0xbcb8aa3b, v155
	v_exp_f32_e32 v6, v6
	v_exp_f32_e32 v7, v7
	v_perm_b32 v4, v5, v4, s68
	v_add_f32_e32 v5, 1.0, v6
	v_add_f32_e32 v6, 1.0, v7
	v_mul_f32_e32 v7, 0xbcb8aa3b, v156
	v_mul_f32_e32 v8, 0xbcb8aa3b, v157
	v_exp_f32_e32 v7, v7
	v_exp_f32_e32 v8, v8
	v_rcp_f32_e32 v5, v5
	v_rcp_f32_e32 v6, v6
	v_add_f32_e32 v7, 1.0, v7
	v_add_f32_e32 v8, 1.0, v8
	v_rcp_f32_e32 v7, v7
	v_rcp_f32_e32 v8, v8
	v_fmamk_f32 v5, v5, 0x437f0000, v196
	v_fmamk_f32 v6, v6, 0x437f0000, v196
	v_fmamk_f32 v7, v7, 0x437f0000, v196
	v_fmamk_f32 v8, v8, 0x437f0000, v196
	v_perm_b32 v5, v6, v5, s67
	v_perm_b32 v6, v8, v7, s67
	v_mul_f32_e32 v7, 0xbcb8aa3b, v150
	v_mul_f32_e32 v8, 0xbcb8aa3b, v151
	v_exp_f32_e32 v7, v7
	v_exp_f32_e32 v8, v8
	v_perm_b32 v5, v6, v5, s68
	v_add_f32_e32 v6, 1.0, v7
	v_add_f32_e32 v7, 1.0, v8
	v_mul_f32_e32 v8, 0xbcb8aa3b, v152
	v_mul_f32_e32 v9, 0xbcb8aa3b, v153
	v_exp_f32_e32 v8, v8
	v_exp_f32_e32 v9, v9
	v_rcp_f32_e32 v6, v6
	v_rcp_f32_e32 v7, v7
	v_add_f32_e32 v8, 1.0, v8
	v_add_f32_e32 v9, 1.0, v9
	v_rcp_f32_e32 v8, v8
	v_rcp_f32_e32 v9, v9
	v_fmamk_f32 v6, v6, 0x437f0000, v196
	v_fmamk_f32 v7, v7, 0x437f0000, v196
	v_fmamk_f32 v8, v8, 0x437f0000, v196
	v_fmamk_f32 v9, v9, 0x437f0000, v196
	v_perm_b32 v6, v7, v6, s67
	v_perm_b32 v7, v9, v8, s67
	v_mul_f32_e32 v8, 0xbcb8aa3b, v146
	v_mul_f32_e32 v9, 0xbcb8aa3b, v147
	v_exp_f32_e32 v8, v8
	v_exp_f32_e32 v9, v9
	v_perm_b32 v6, v7, v6, s68
	v_add_f32_e32 v7, 1.0, v8
	v_add_f32_e32 v8, 1.0, v9
	v_mul_f32_e32 v9, 0xbcb8aa3b, v148
	v_mul_f32_e32 v10, 0xbcb8aa3b, v149
	v_exp_f32_e32 v9, v9
	v_exp_f32_e32 v10, v10
	v_rcp_f32_e32 v7, v7
	v_rcp_f32_e32 v8, v8
	v_add_f32_e32 v9, 1.0, v9
	v_add_f32_e32 v10, 1.0, v10
	v_rcp_f32_e32 v9, v9
	v_rcp_f32_e32 v10, v10
	s_cmp_lt_i32 s73, 8
	v_ashrrev_i32_e32 v3, 31, v2
	s_cselect_b32 s25, s41, s59
	s_cselect_b32 s24, s40, s53
	v_lshlrev_b64 v[2:3], 11, v[2:3]
	s_lshl_b32 s8, s73, 8
	v_lshl_add_u64 v[2:3], s[24:25], 0, v[2:3]
	s_and_b32 s8, s8, 0x700
	v_lshl_add_u64 v[2:3], v[2:3], 0, s[8:9]
	v_fmamk_f32 v7, v7, 0x437f0000, v196
	v_fmamk_f32 v8, v8, 0x437f0000, v196
	v_fmamk_f32 v9, v9, 0x437f0000, v196
	v_fmamk_f32 v10, v10, 0x437f0000, v196
	v_lshl_add_u64 v[2:3], v[2:3], 0, s[14:15]
	v_perm_b32 v7, v8, v7, s67
	v_perm_b32 v8, v10, v9, s67
	v_lshl_add_u64 v[2:3], v[2:3], 0, v[162:163]
	v_perm_b32 v7, v8, v7, s68
	global_store_dwordx4 v[2:3], v[4:7], off
	v_mul_f32_e32 v8, 0xbcb8aa3b, v142
	v_mul_f32_e32 v9, 0xbcb8aa3b, v143
	v_mul_f32_e32 v6, 0xbcb8aa3b, v144
	v_mul_f32_e32 v7, 0xbcb8aa3b, v145
	v_exp_f32_e32 v8, v8
	v_exp_f32_e32 v9, v9
	v_exp_f32_e32 v6, v6
	v_exp_f32_e32 v7, v7
	v_add_f32_e32 v4, 1.0, v8
	v_add_f32_e32 v5, 1.0, v9
	v_add_f32_e32 v6, 1.0, v6
	v_add_f32_e32 v7, 1.0, v7
	v_rcp_f32_e32 v4, v4
	v_rcp_f32_e32 v5, v5
	v_rcp_f32_e32 v6, v6
	v_rcp_f32_e32 v7, v7
	v_fmamk_f32 v4, v4, 0x437f0000, v196
	v_fmamk_f32 v5, v5, 0x437f0000, v196
	v_fmamk_f32 v6, v6, 0x437f0000, v196
	v_fmamk_f32 v7, v7, 0x437f0000, v196
	v_perm_b32 v4, v5, v4, s67
	v_perm_b32 v5, v7, v6, s67
	v_mul_f32_e32 v6, 0xbcb8aa3b, v138
	v_mul_f32_e32 v7, 0xbcb8aa3b, v139
	v_exp_f32_e32 v6, v6
	v_exp_f32_e32 v7, v7
	v_perm_b32 v4, v5, v4, s68
	v_add_f32_e32 v5, 1.0, v6
	v_add_f32_e32 v6, 1.0, v7
	v_mul_f32_e32 v7, 0xbcb8aa3b, v140
	v_mul_f32_e32 v8, 0xbcb8aa3b, v141
	v_exp_f32_e32 v7, v7
	v_exp_f32_e32 v8, v8
	v_rcp_f32_e32 v5, v5
	v_rcp_f32_e32 v6, v6
	v_add_f32_e32 v7, 1.0, v7
	v_add_f32_e32 v8, 1.0, v8
	v_rcp_f32_e32 v7, v7
	v_rcp_f32_e32 v8, v8
	v_fmamk_f32 v5, v5, 0x437f0000, v196
	v_fmamk_f32 v6, v6, 0x437f0000, v196
	v_fmamk_f32 v7, v7, 0x437f0000, v196
	v_fmamk_f32 v8, v8, 0x437f0000, v196
	v_perm_b32 v5, v6, v5, s67
	v_perm_b32 v6, v8, v7, s67
	v_mul_f32_e32 v7, 0xbcb8aa3b, v134
	v_mul_f32_e32 v8, 0xbcb8aa3b, v135
	v_exp_f32_e32 v7, v7
	v_exp_f32_e32 v8, v8
	v_perm_b32 v5, v6, v5, s68
	v_add_f32_e32 v6, 1.0, v7
	v_add_f32_e32 v7, 1.0, v8
	v_mul_f32_e32 v8, 0xbcb8aa3b, v136
	v_mul_f32_e32 v9, 0xbcb8aa3b, v137
	v_exp_f32_e32 v8, v8
	v_exp_f32_e32 v9, v9
	v_rcp_f32_e32 v6, v6
	v_rcp_f32_e32 v7, v7
	v_add_f32_e32 v8, 1.0, v8
	v_add_f32_e32 v9, 1.0, v9
	v_rcp_f32_e32 v8, v8
	v_rcp_f32_e32 v9, v9
	v_fmamk_f32 v6, v6, 0x437f0000, v196
	v_fmamk_f32 v7, v7, 0x437f0000, v196
	v_fmamk_f32 v8, v8, 0x437f0000, v196
	v_fmamk_f32 v9, v9, 0x437f0000, v196
	v_perm_b32 v6, v7, v6, s67
	v_perm_b32 v7, v9, v8, s67
	v_mul_f32_e32 v8, 0xbcb8aa3b, v130
	v_mul_f32_e32 v9, 0xbcb8aa3b, v131
	v_exp_f32_e32 v8, v8
	v_exp_f32_e32 v9, v9
	v_perm_b32 v6, v7, v6, s68
	v_add_f32_e32 v7, 1.0, v8
	v_add_f32_e32 v8, 1.0, v9
	v_mul_f32_e32 v9, 0xbcb8aa3b, v132
	v_mul_f32_e32 v10, 0xbcb8aa3b, v133
	v_exp_f32_e32 v9, v9
	v_exp_f32_e32 v10, v10
	v_rcp_f32_e32 v7, v7
	v_rcp_f32_e32 v8, v8
	v_add_f32_e32 v9, 1.0, v9
	v_add_f32_e32 v10, 1.0, v10
	v_rcp_f32_e32 v9, v9
	v_rcp_f32_e32 v10, v10
	v_fmamk_f32 v7, v7, 0x437f0000, v196
; __device__ __forceinline__ float fsigmoid(float x) { return __builtin_amdgcn_rcpf(1.0f + __builtin_amdgcn_exp2f(-1.44269504f * x)); }
; __device__ __forceinline__ unsigned pk4_u8(float a, float b, float c, float d) {
;     const unsigned ya = __builtin_bit_cast(unsigned, a * 255.0f + 8388608.0f), yb = __builtin_bit_cast(unsigned, b * 255.0f + 8388608.0f), yc = __builtin_bit_cast(unsigned, c * 255.0f + 8388608.0f), yd = __builtin_bit_cast(unsigned, d * 255.0f + 8388608.0f);
;     const unsigned w01 = __builtin_amdgcn_perm(yb, ya, 0x0c0c0400u), w23 = __builtin_amdgcn_perm(yd, yc, 0x0c0c0400u);
;     return __builtin_amdgcn_perm(w23, w01, 0x05040100u); }
;     __device__ __forceinline__ void operator()(AccRef acc, const GUnit& u, int wr, int wc, int fr, int fq) const {
;     ...
;             for (int m = 0; m < 4; ++m) { u32x4 w;
; #pragma unroll
;                 for (int bj = 0; bj < 2; ++bj)
; #pragma unroll
;                     for (int n = 0; n < 2; ++n) { const f32x4 v = acc[ai][bj][m][n]; w[bj * 2 + n] = pk4_u8(fsigmoid(v[0] * W8_INV), fsigmoid(v[1] * W8_INV), fsigmoid(v[2] * W8_INV), fsigmoid(v[3] * W8_INV)); }
;                 *(u32x4*)(base + (size_t)(ai * 128 + m * 16) * D) = w; }
	v_fmamk_f32 v8, v8, 0x437f0000, v196
	v_fmamk_f32 v9, v9, 0x437f0000, v196
	v_fmamk_f32 v10, v10, 0x437f0000, v196
	v_perm_b32 v7, v8, v7, s67
	v_perm_b32 v8, v10, v9, s67
	v_perm_b32 v7, v8, v7, s68
	v_add_co_u32_e32 v8, vcc, s63, v2
	s_nop 0
	s_nop 0
	v_addc_co_u32_e32 v9, vcc, 0, v3, vcc
	global_store_dwordx4 v[8:9], v[4:7], off
	v_mul_f32_e32 v10, 0xbcb8aa3b, v126
	v_mul_f32_e32 v11, 0xbcb8aa3b, v127
	v_mul_f32_e32 v6, 0xbcb8aa3b, v128
	v_mul_f32_e32 v7, 0xbcb8aa3b, v129
	v_exp_f32_e32 v10, v10
	v_exp_f32_e32 v11, v11
	v_exp_f32_e32 v6, v6
	v_exp_f32_e32 v7, v7
	v_add_f32_e32 v4, 1.0, v10
	v_add_f32_e32 v5, 1.0, v11
	v_add_f32_e32 v6, 1.0, v6
	v_add_f32_e32 v7, 1.0, v7
	v_rcp_f32_e32 v4, v4
	v_rcp_f32_e32 v5, v5
	v_rcp_f32_e32 v6, v6
	v_rcp_f32_e32 v7, v7
	v_fmamk_f32 v4, v4, 0x437f0000, v196
	v_fmamk_f32 v5, v5, 0x437f0000, v196
	v_fmamk_f32 v6, v6, 0x437f0000, v196
	v_fmamk_f32 v7, v7, 0x437f0000, v196
	v_perm_b32 v4, v5, v4, s67
	v_perm_b32 v5, v7, v6, s67
	v_mul_f32_e32 v6, 0xbcb8aa3b, v122
	v_mul_f32_e32 v7, 0xbcb8aa3b, v123
	v_exp_f32_e32 v6, v6
	v_exp_f32_e32 v7, v7
	v_perm_b32 v4, v5, v4, s68
	v_add_f32_e32 v5, 1.0, v6
	v_add_f32_e32 v6, 1.0, v7
	v_mul_f32_e32 v7, 0xbcb8aa3b, v124
	v_mul_f32_e32 v8, 0xbcb8aa3b, v125
	v_exp_f32_e32 v7, v7
	v_exp_f32_e32 v8, v8
	v_rcp_f32_e32 v5, v5
	v_rcp_f32_e32 v6, v6
	v_add_f32_e32 v7, 1.0, v7
	v_add_f32_e32 v8, 1.0, v8
	v_rcp_f32_e32 v7, v7
	v_rcp_f32_e32 v8, v8
	v_fmamk_f32 v5, v5, 0x437f0000, v196
	v_fmamk_f32 v6, v6, 0x437f0000, v196
	v_fmamk_f32 v7, v7, 0x437f0000, v196
	v_fmamk_f32 v8, v8, 0x437f0000, v196
	v_perm_b32 v5, v6, v5, s67
	v_perm_b32 v6, v8, v7, s67
	v_mul_f32_e32 v7, 0xbcb8aa3b, v118
	v_mul_f32_e32 v8, 0xbcb8aa3b, v119
	v_exp_f32_e32 v7, v7
	v_exp_f32_e32 v8, v8
	v_perm_b32 v5, v6, v5, s68
	v_add_f32_e32 v6, 1.0, v7
	v_add_f32_e32 v7, 1.0, v8
	v_mul_f32_e32 v8, 0xbcb8aa3b, v120
	v_mul_f32_e32 v9, 0xbcb8aa3b, v121
	v_exp_f32_e32 v8, v8
	v_exp_f32_e32 v9, v9
	v_rcp_f32_e32 v6, v6
	v_rcp_f32_e32 v7, v7
	v_add_f32_e32 v8, 1.0, v8
	v_add_f32_e32 v9, 1.0, v9
	v_rcp_f32_e32 v8, v8
	v_rcp_f32_e32 v9, v9
	v_fmamk_f32 v6, v6, 0x437f0000, v196
	v_fmamk_f32 v7, v7, 0x437f0000, v196
	v_fmamk_f32 v8, v8, 0x437f0000, v196
	v_fmamk_f32 v9, v9, 0x437f0000, v196
	v_perm_b32 v6, v7, v6, s67
	v_perm_b32 v7, v9, v8, s67
	v_mul_f32_e32 v8, 0xbcb8aa3b, v114
	v_mul_f32_e32 v9, 0xbcb8aa3b, v115
	v_exp_f32_e32 v8, v8
	v_exp_f32_e32 v9, v9
	v_perm_b32 v6, v7, v6, s68
	v_add_f32_e32 v7, 1.0, v8
	v_add_f32_e32 v8, 1.0, v9
	v_mul_f32_e32 v9, 0xbcb8aa3b, v116
	v_mul_f32_e32 v10, 0xbcb8aa3b, v117
	v_exp_f32_e32 v9, v9
	v_exp_f32_e32 v10, v10
	v_rcp_f32_e32 v7, v7
	v_rcp_f32_e32 v8, v8
	v_add_f32_e32 v9, 1.0, v9
	v_add_f32_e32 v10, 1.0, v10
	v_rcp_f32_e32 v9, v9
	v_rcp_f32_e32 v10, v10
	v_fmamk_f32 v7, v7, 0x437f0000, v196
	v_fmamk_f32 v8, v8, 0x437f0000, v196
	v_fmamk_f32 v9, v9, 0x437f0000, v196
	v_fmamk_f32 v10, v10, 0x437f0000, v196
	v_perm_b32 v7, v8, v7, s67
	v_perm_b32 v8, v10, v9, s67
	v_perm_b32 v7, v8, v7, s68
	v_add_co_u32_e32 v8, vcc, s52, v2
	s_nop 0
	s_nop 0
	v_addc_co_u32_e32 v9, vcc, 0, v3, vcc
	global_store_dwordx4 v[8:9], v[4:7], off
	v_mul_f32_e32 v10, 0xbcb8aa3b, v110
	v_mul_f32_e32 v11, 0xbcb8aa3b, v111
	v_mul_f32_e32 v6, 0xbcb8aa3b, v112
	v_mul_f32_e32 v7, 0xbcb8aa3b, v113
	v_exp_f32_e32 v10, v10
	v_exp_f32_e32 v11, v11
	v_exp_f32_e32 v6, v6
	v_exp_f32_e32 v7, v7
	v_add_f32_e32 v4, 1.0, v10
	v_add_f32_e32 v5, 1.0, v11
	v_add_f32_e32 v6, 1.0, v6
	v_add_f32_e32 v7, 1.0, v7
	v_rcp_f32_e32 v4, v4
	v_rcp_f32_e32 v5, v5
	v_rcp_f32_e32 v6, v6
	v_rcp_f32_e32 v7, v7
	v_fmamk_f32 v4, v4, 0x437f0000, v196
	v_fmamk_f32 v5, v5, 0x437f0000, v196
	v_fmamk_f32 v6, v6, 0x437f0000, v196
	v_fmamk_f32 v7, v7, 0x437f0000, v196
	v_perm_b32 v4, v5, v4, s67
	v_perm_b32 v5, v7, v6, s67
	v_mul_f32_e32 v6, 0xbcb8aa3b, v106
	v_mul_f32_e32 v7, 0xbcb8aa3b, v107
	v_exp_f32_e32 v6, v6
	v_exp_f32_e32 v7, v7
	v_perm_b32 v4, v5, v4, s68
	v_add_f32_e32 v5, 1.0, v6
	v_add_f32_e32 v6, 1.0, v7
	v_mul_f32_e32 v7, 0xbcb8aa3b, v108
	v_mul_f32_e32 v8, 0xbcb8aa3b, v109
	v_exp_f32_e32 v7, v7
	v_exp_f32_e32 v8, v8
	v_rcp_f32_e32 v5, v5
	v_rcp_f32_e32 v6, v6
	v_add_f32_e32 v7, 1.0, v7
	v_add_f32_e32 v8, 1.0, v8
	v_rcp_f32_e32 v7, v7
	v_rcp_f32_e32 v8, v8
	v_fmamk_f32 v5, v5, 0x437f0000, v196
	v_fmamk_f32 v6, v6, 0x437f0000, v196
	v_fmamk_f32 v7, v7, 0x437f0000, v196
	v_fmamk_f32 v8, v8, 0x437f0000, v196
	v_perm_b32 v5, v6, v5, s67
	v_perm_b32 v6, v8, v7, s67
	v_mul_f32_e32 v7, 0xbcb8aa3b, v102
	v_mul_f32_e32 v8, 0xbcb8aa3b, v103
	v_exp_f32_e32 v7, v7
	v_exp_f32_e32 v8, v8
	v_perm_b32 v5, v6, v5, s68
	v_add_f32_e32 v6, 1.0, v7
	v_add_f32_e32 v7, 1.0, v8
	v_mul_f32_e32 v8, 0xbcb8aa3b, v104
	v_mul_f32_e32 v9, 0xbcb8aa3b, v105
	v_exp_f32_e32 v8, v8
	v_exp_f32_e32 v9, v9
	v_rcp_f32_e32 v6, v6
	v_rcp_f32_e32 v7, v7
	v_add_f32_e32 v8, 1.0, v8
	v_add_f32_e32 v9, 1.0, v9
	v_rcp_f32_e32 v8, v8
	v_rcp_f32_e32 v9, v9
	v_fmamk_f32 v6, v6, 0x437f0000, v196
	v_fmamk_f32 v7, v7, 0x437f0000, v196
	v_fmamk_f32 v8, v8, 0x437f0000, v196
	v_fmamk_f32 v9, v9, 0x437f0000, v196
	v_perm_b32 v6, v7, v6, s67
	v_perm_b32 v7, v9, v8, s67
	v_mul_f32_e32 v8, 0xbcb8aa3b, v98
	v_mul_f32_e32 v9, 0xbcb8aa3b, v99
	v_exp_f32_e32 v8, v8
	v_exp_f32_e32 v9, v9
	v_perm_b32 v6, v7, v6, s68
	v_add_f32_e32 v7, 1.0, v8
	v_add_f32_e32 v8, 1.0, v9
	v_mul_f32_e32 v9, 0xbcb8aa3b, v100
	v_mul_f32_e32 v10, 0xbcb8aa3b, v101
	v_exp_f32_e32 v9, v9
	v_exp_f32_e32 v10, v10
	v_rcp_f32_e32 v7, v7
	v_rcp_f32_e32 v8, v8
	v_add_f32_e32 v9, 1.0, v9
	v_add_f32_e32 v10, 1.0, v10
	v_rcp_f32_e32 v9, v9
	v_rcp_f32_e32 v10, v10
	v_fmamk_f32 v7, v7, 0x437f0000, v196
	v_fmamk_f32 v8, v8, 0x437f0000, v196
; __device__ __forceinline__ float fsigmoid(float x) { return __builtin_amdgcn_rcpf(1.0f + __builtin_amdgcn_exp2f(-1.44269504f * x)); }
; __device__ __forceinline__ unsigned pk4_u8(float a, float b, float c, float d) {
;     const unsigned ya = __builtin_bit_cast(unsigned, a * 255.0f + 8388608.0f), yb = __builtin_bit_cast(unsigned, b * 255.0f + 8388608.0f), yc = __builtin_bit_cast(unsigned, c * 255.0f + 8388608.0f), yd = __builtin_bit_cast(unsigned, d * 255.0f + 8388608.0f);
;     const unsigned w01 = __builtin_amdgcn_perm(yb, ya, 0x0c0c0400u), w23 = __builtin_amdgcn_perm(yd, yc, 0x0c0c0400u);
;     return __builtin_amdgcn_perm(w23, w01, 0x05040100u); }
;     __device__ __forceinline__ void operator()(AccRef acc, const GUnit& u, int wr, int wc, int fr, int fq) const {
;     ...
;             for (int m = 0; m < 4; ++m) { u32x4 w;
; #pragma unroll
;                 for (int bj = 0; bj < 2; ++bj)
; #pragma unroll
;                     for (int n = 0; n < 2; ++n) { const f32x4 v = acc[ai][bj][m][n]; w[bj * 2 + n] = pk4_u8(fsigmoid(v[0] * W8_INV), fsigmoid(v[1] * W8_INV), fsigmoid(v[2] * W8_INV), fsigmoid(v[3] * W8_INV)); }
;                 *(u32x4*)(base + (size_t)(ai * 128 + m * 16) * D) = w; }
	v_fmamk_f32 v9, v9, 0x437f0000, v196
	v_fmamk_f32 v10, v10, 0x437f0000, v196
	v_perm_b32 v7, v8, v7, s67
	v_perm_b32 v8, v10, v9, s67
	v_perm_b32 v7, v8, v7, s68
	v_add_co_u32_e32 v8, vcc, s62, v2
	s_nop 0
	s_nop 0
	v_addc_co_u32_e32 v9, vcc, 0, v3, vcc
	global_store_dwordx4 v[8:9], v[4:7], off
	v_mul_f32_e32 v10, 0xbcb8aa3b, v94
	v_mul_f32_e32 v11, 0xbcb8aa3b, v95
	v_mul_f32_e32 v6, 0xbcb8aa3b, v96
	v_mul_f32_e32 v7, 0xbcb8aa3b, v97
	v_exp_f32_e32 v10, v10
	v_exp_f32_e32 v11, v11
	v_exp_f32_e32 v6, v6
	v_exp_f32_e32 v7, v7
	v_add_f32_e32 v4, 1.0, v10
	v_add_f32_e32 v5, 1.0, v11
	v_add_f32_e32 v6, 1.0, v6
	v_add_f32_e32 v7, 1.0, v7
	v_rcp_f32_e32 v4, v4
	v_rcp_f32_e32 v5, v5
	v_rcp_f32_e32 v6, v6
	v_rcp_f32_e32 v7, v7
	v_fmamk_f32 v4, v4, 0x437f0000, v196
	v_fmamk_f32 v5, v5, 0x437f0000, v196
	v_fmamk_f32 v6, v6, 0x437f0000, v196
	v_fmamk_f32 v7, v7, 0x437f0000, v196
	v_perm_b32 v4, v5, v4, s67
	v_perm_b32 v5, v7, v6, s67
	v_mul_f32_e32 v6, 0xbcb8aa3b, v90
	v_mul_f32_e32 v7, 0xbcb8aa3b, v91
	v_exp_f32_e32 v6, v6
	v_exp_f32_e32 v7, v7
	v_perm_b32 v4, v5, v4, s68
	v_add_f32_e32 v5, 1.0, v6
	v_add_f32_e32 v6, 1.0, v7
	v_mul_f32_e32 v7, 0xbcb8aa3b, v92
	v_mul_f32_e32 v8, 0xbcb8aa3b, v93
	v_exp_f32_e32 v7, v7
	v_exp_f32_e32 v8, v8
	v_rcp_f32_e32 v5, v5
	v_rcp_f32_e32 v6, v6
	v_add_f32_e32 v7, 1.0, v7
	v_add_f32_e32 v8, 1.0, v8
	v_rcp_f32_e32 v7, v7
	v_rcp_f32_e32 v8, v8
	v_fmamk_f32 v5, v5, 0x437f0000, v196
	v_fmamk_f32 v6, v6, 0x437f0000, v196
	v_fmamk_f32 v7, v7, 0x437f0000, v196
	v_fmamk_f32 v8, v8, 0x437f0000, v196
	v_perm_b32 v5, v6, v5, s67
	v_perm_b32 v6, v8, v7, s67
	v_mul_f32_e32 v7, 0xbcb8aa3b, v86
	v_mul_f32_e32 v8, 0xbcb8aa3b, v87
	v_exp_f32_e32 v7, v7
	v_exp_f32_e32 v8, v8
	v_perm_b32 v5, v6, v5, s68
	v_add_f32_e32 v6, 1.0, v7
	v_add_f32_e32 v7, 1.0, v8
	v_mul_f32_e32 v8, 0xbcb8aa3b, v88
	v_mul_f32_e32 v9, 0xbcb8aa3b, v89
	v_exp_f32_e32 v8, v8
	v_exp_f32_e32 v9, v9
	v_rcp_f32_e32 v6, v6
	v_rcp_f32_e32 v7, v7
	v_add_f32_e32 v8, 1.0, v8
	v_add_f32_e32 v9, 1.0, v9
	v_rcp_f32_e32 v8, v8
	v_rcp_f32_e32 v9, v9
	v_fmamk_f32 v6, v6, 0x437f0000, v196
	v_fmamk_f32 v7, v7, 0x437f0000, v196
	v_fmamk_f32 v8, v8, 0x437f0000, v196
	v_fmamk_f32 v9, v9, 0x437f0000, v196
	v_perm_b32 v6, v7, v6, s67
	v_perm_b32 v7, v9, v8, s67
	v_mul_f32_e32 v8, 0xbcb8aa3b, v82
	v_mul_f32_e32 v9, 0xbcb8aa3b, v83
	v_exp_f32_e32 v8, v8
	v_exp_f32_e32 v9, v9
	v_perm_b32 v6, v7, v6, s68
	v_add_f32_e32 v7, 1.0, v8
	v_add_f32_e32 v8, 1.0, v9
	v_mul_f32_e32 v9, 0xbcb8aa3b, v84
	v_mul_f32_e32 v10, 0xbcb8aa3b, v85
	v_exp_f32_e32 v9, v9
	v_exp_f32_e32 v10, v10
	v_rcp_f32_e32 v7, v7
	v_rcp_f32_e32 v8, v8
	v_add_f32_e32 v9, 1.0, v9
	v_add_f32_e32 v10, 1.0, v10
	v_rcp_f32_e32 v9, v9
	v_rcp_f32_e32 v10, v10
	v_fmamk_f32 v7, v7, 0x437f0000, v196
	v_fmamk_f32 v8, v8, 0x437f0000, v196
	v_fmamk_f32 v9, v9, 0x437f0000, v196
	v_fmamk_f32 v10, v10, 0x437f0000, v196
	v_perm_b32 v7, v8, v7, s67
	v_perm_b32 v8, v10, v9, s67
	v_perm_b32 v7, v8, v7, s68
	v_add_co_u32_e32 v8, vcc, s69, v2
	s_nop 0
	s_nop 0
	v_addc_co_u32_e32 v9, vcc, 0, v3, vcc
	global_store_dwordx4 v[8:9], v[4:7], off
	v_mul_f32_e32 v10, 0xbcb8aa3b, v78
	v_mul_f32_e32 v11, 0xbcb8aa3b, v79
	v_mul_f32_e32 v6, 0xbcb8aa3b, v80
	v_mul_f32_e32 v7, 0xbcb8aa3b, v81
	v_exp_f32_e32 v10, v10
	v_exp_f32_e32 v11, v11
	v_exp_f32_e32 v6, v6
	v_exp_f32_e32 v7, v7
	v_add_f32_e32 v4, 1.0, v10
	v_add_f32_e32 v5, 1.0, v11
	v_add_f32_e32 v6, 1.0, v6
	v_add_f32_e32 v7, 1.0, v7
	v_rcp_f32_e32 v4, v4
	v_rcp_f32_e32 v5, v5
	v_rcp_f32_e32 v6, v6
	v_rcp_f32_e32 v7, v7
	v_fmamk_f32 v4, v4, 0x437f0000, v196
	v_fmamk_f32 v5, v5, 0x437f0000, v196
	v_fmamk_f32 v6, v6, 0x437f0000, v196
	v_fmamk_f32 v7, v7, 0x437f0000, v196
	v_perm_b32 v4, v5, v4, s67
	v_perm_b32 v5, v7, v6, s67
	v_mul_f32_e32 v6, 0xbcb8aa3b, v74
	v_mul_f32_e32 v7, 0xbcb8aa3b, v75
	v_exp_f32_e32 v6, v6
	v_exp_f32_e32 v7, v7
	v_perm_b32 v4, v5, v4, s68
	v_add_f32_e32 v5, 1.0, v6
	v_add_f32_e32 v6, 1.0, v7
	v_mul_f32_e32 v7, 0xbcb8aa3b, v76
	v_mul_f32_e32 v8, 0xbcb8aa3b, v77
	v_exp_f32_e32 v7, v7
	v_exp_f32_e32 v8, v8
	v_rcp_f32_e32 v5, v5
	v_rcp_f32_e32 v6, v6
	v_add_f32_e32 v7, 1.0, v7
	v_add_f32_e32 v8, 1.0, v8
	v_rcp_f32_e32 v7, v7
	v_rcp_f32_e32 v8, v8
	v_fmamk_f32 v5, v5, 0x437f0000, v196
	v_fmamk_f32 v6, v6, 0x437f0000, v196
	v_fmamk_f32 v7, v7, 0x437f0000, v196
	v_fmamk_f32 v8, v8, 0x437f0000, v196
	v_perm_b32 v5, v6, v5, s67
	v_perm_b32 v6, v8, v7, s67
	v_mul_f32_e32 v7, 0xbcb8aa3b, v70
	v_mul_f32_e32 v8, 0xbcb8aa3b, v71
	v_exp_f32_e32 v7, v7
	v_exp_f32_e32 v8, v8
	v_perm_b32 v5, v6, v5, s68
	v_add_f32_e32 v6, 1.0, v7
	v_add_f32_e32 v7, 1.0, v8
	v_mul_f32_e32 v8, 0xbcb8aa3b, v72
	v_mul_f32_e32 v9, 0xbcb8aa3b, v73
	v_exp_f32_e32 v8, v8
	v_exp_f32_e32 v9, v9
	v_rcp_f32_e32 v6, v6
	v_rcp_f32_e32 v7, v7
	v_add_f32_e32 v8, 1.0, v8
	v_add_f32_e32 v9, 1.0, v9
	v_rcp_f32_e32 v8, v8
	v_rcp_f32_e32 v9, v9
	v_fmamk_f32 v6, v6, 0x437f0000, v196
	v_fmamk_f32 v7, v7, 0x437f0000, v196
	v_fmamk_f32 v8, v8, 0x437f0000, v196
	v_fmamk_f32 v9, v9, 0x437f0000, v196
	v_perm_b32 v6, v7, v6, s67
	v_perm_b32 v7, v9, v8, s67
	v_mul_f32_e32 v8, 0xbcb8aa3b, v66
	v_mul_f32_e32 v9, 0xbcb8aa3b, v67
	v_exp_f32_e32 v8, v8
	v_exp_f32_e32 v9, v9
	v_perm_b32 v6, v7, v6, s68
	v_add_f32_e32 v7, 1.0, v8
	v_add_f32_e32 v8, 1.0, v9
	v_mul_f32_e32 v9, 0xbcb8aa3b, v68
	v_mul_f32_e32 v10, 0xbcb8aa3b, v69
	v_exp_f32_e32 v9, v9
	v_exp_f32_e32 v10, v10
	v_rcp_f32_e32 v7, v7
	v_rcp_f32_e32 v8, v8
	v_add_f32_e32 v9, 1.0, v9
	v_add_f32_e32 v10, 1.0, v10
	v_rcp_f32_e32 v9, v9
	v_rcp_f32_e32 v10, v10
	v_fmamk_f32 v7, v7, 0x437f0000, v196
	v_fmamk_f32 v8, v8, 0x437f0000, v196
	v_fmamk_f32 v9, v9, 0x437f0000, v196
; __device__ __forceinline__ float fsigmoid(float x) { return __builtin_amdgcn_rcpf(1.0f + __builtin_amdgcn_exp2f(-1.44269504f * x)); }
; __device__ __forceinline__ unsigned pk4_u8(float a, float b, float c, float d) {
;     const unsigned ya = __builtin_bit_cast(unsigned, a * 255.0f + 8388608.0f), yb = __builtin_bit_cast(unsigned, b * 255.0f + 8388608.0f), yc = __builtin_bit_cast(unsigned, c * 255.0f + 8388608.0f), yd = __builtin_bit_cast(unsigned, d * 255.0f + 8388608.0f);
;     const unsigned w01 = __builtin_amdgcn_perm(yb, ya, 0x0c0c0400u), w23 = __builtin_amdgcn_perm(yd, yc, 0x0c0c0400u);
;     return __builtin_amdgcn_perm(w23, w01, 0x05040100u); }
;     __device__ __forceinline__ void operator()(AccRef acc, const GUnit& u, int wr, int wc, int fr, int fq) const {
;     ...
;             for (int m = 0; m < 4; ++m) { u32x4 w;
; #pragma unroll
;                 for (int bj = 0; bj < 2; ++bj)
; #pragma unroll
;                     for (int n = 0; n < 2; ++n) { const f32x4 v = acc[ai][bj][m][n]; w[bj * 2 + n] = pk4_u8(fsigmoid(v[0] * W8_INV), fsigmoid(v[1] * W8_INV), fsigmoid(v[2] * W8_INV), fsigmoid(v[3] * W8_INV)); }
;                 *(u32x4*)(base + (size_t)(ai * 128 + m * 16) * D) = w; }
	v_fmamk_f32 v10, v10, 0x437f0000, v196
	v_perm_b32 v7, v8, v7, s67
	v_perm_b32 v8, v10, v9, s67
	v_perm_b32 v7, v8, v7, s68
	v_add_co_u32_e32 v8, vcc, s70, v2
	s_nop 0
	s_nop 0
	v_addc_co_u32_e32 v9, vcc, 0, v3, vcc
	global_store_dwordx4 v[8:9], v[4:7], off
	v_mul_f32_e32 v10, 0xbcb8aa3b, v62
	v_mul_f32_e32 v11, 0xbcb8aa3b, v63
	v_mul_f32_e32 v6, 0xbcb8aa3b, v64
	v_mul_f32_e32 v7, 0xbcb8aa3b, v65
	v_exp_f32_e32 v10, v10
	v_exp_f32_e32 v11, v11
	v_exp_f32_e32 v6, v6
	v_exp_f32_e32 v7, v7
	v_add_f32_e32 v4, 1.0, v10
	v_add_f32_e32 v5, 1.0, v11
	v_add_f32_e32 v6, 1.0, v6
	v_add_f32_e32 v7, 1.0, v7
	v_rcp_f32_e32 v4, v4
	v_rcp_f32_e32 v5, v5
	v_rcp_f32_e32 v6, v6
	v_rcp_f32_e32 v7, v7
	v_fmamk_f32 v4, v4, 0x437f0000, v196
	v_fmamk_f32 v5, v5, 0x437f0000, v196
	v_fmamk_f32 v6, v6, 0x437f0000, v196
	v_fmamk_f32 v7, v7, 0x437f0000, v196
	v_perm_b32 v4, v5, v4, s67
	v_perm_b32 v5, v7, v6, s67
	v_mul_f32_e32 v6, 0xbcb8aa3b, v58
	v_mul_f32_e32 v7, 0xbcb8aa3b, v59
	v_exp_f32_e32 v6, v6
	v_exp_f32_e32 v7, v7
	v_perm_b32 v4, v5, v4, s68
	v_add_f32_e32 v5, 1.0, v6
	v_add_f32_e32 v6, 1.0, v7
	v_mul_f32_e32 v7, 0xbcb8aa3b, v60
	v_mul_f32_e32 v8, 0xbcb8aa3b, v61
	v_exp_f32_e32 v7, v7
	v_exp_f32_e32 v8, v8
	v_rcp_f32_e32 v5, v5
	v_rcp_f32_e32 v6, v6
	v_add_f32_e32 v7, 1.0, v7
	v_add_f32_e32 v8, 1.0, v8
	v_rcp_f32_e32 v7, v7
	v_rcp_f32_e32 v8, v8
	v_fmamk_f32 v5, v5, 0x437f0000, v196
	v_fmamk_f32 v6, v6, 0x437f0000, v196
	v_fmamk_f32 v7, v7, 0x437f0000, v196
	v_fmamk_f32 v8, v8, 0x437f0000, v196
	v_perm_b32 v5, v6, v5, s67
	v_perm_b32 v6, v8, v7, s67
	v_mul_f32_e32 v7, 0xbcb8aa3b, v54
	v_mul_f32_e32 v8, 0xbcb8aa3b, v55
	v_exp_f32_e32 v7, v7
	v_exp_f32_e32 v8, v8
	v_perm_b32 v5, v6, v5, s68
	v_add_f32_e32 v6, 1.0, v7
	v_add_f32_e32 v7, 1.0, v8
	v_mul_f32_e32 v8, 0xbcb8aa3b, v56
	v_mul_f32_e32 v9, 0xbcb8aa3b, v57
	v_exp_f32_e32 v8, v8
	v_exp_f32_e32 v9, v9
	v_rcp_f32_e32 v6, v6
	v_rcp_f32_e32 v7, v7
	v_add_f32_e32 v8, 1.0, v8
	v_add_f32_e32 v9, 1.0, v9
	v_rcp_f32_e32 v8, v8
	v_rcp_f32_e32 v9, v9
	v_fmamk_f32 v6, v6, 0x437f0000, v196
	v_fmamk_f32 v7, v7, 0x437f0000, v196
	v_fmamk_f32 v8, v8, 0x437f0000, v196
	v_fmamk_f32 v9, v9, 0x437f0000, v196
	v_perm_b32 v6, v7, v6, s67
	v_perm_b32 v7, v9, v8, s67
	v_mul_f32_e32 v8, 0xbcb8aa3b, v50
	v_mul_f32_e32 v9, 0xbcb8aa3b, v51
	v_exp_f32_e32 v8, v8
	v_exp_f32_e32 v9, v9
	v_perm_b32 v6, v7, v6, s68
	v_add_f32_e32 v7, 1.0, v8
	v_add_f32_e32 v8, 1.0, v9
	v_mul_f32_e32 v9, 0xbcb8aa3b, v52
	v_mul_f32_e32 v10, 0xbcb8aa3b, v53
	v_exp_f32_e32 v9, v9
	v_exp_f32_e32 v10, v10
	v_rcp_f32_e32 v7, v7
	v_rcp_f32_e32 v8, v8
	v_add_f32_e32 v9, 1.0, v9
	v_add_f32_e32 v10, 1.0, v10
	v_rcp_f32_e32 v9, v9
	v_rcp_f32_e32 v10, v10
	v_fmamk_f32 v7, v7, 0x437f0000, v196
	v_fmamk_f32 v8, v8, 0x437f0000, v196
	v_fmamk_f32 v9, v9, 0x437f0000, v196
	v_fmamk_f32 v10, v10, 0x437f0000, v196
	v_perm_b32 v7, v8, v7, s67
	v_perm_b32 v8, v10, v9, s67
	v_perm_b32 v7, v8, v7, s68
	v_add_co_u32_e32 v8, vcc, s71, v2
	s_nop 0
	s_nop 0
	v_addc_co_u32_e32 v9, vcc, 0, v3, vcc
	global_store_dwordx4 v[8:9], v[4:7], off
	v_mul_f32_e32 v10, 0xbcb8aa3b, v46
	v_mul_f32_e32 v11, 0xbcb8aa3b, v47
	v_mul_f32_e32 v6, 0xbcb8aa3b, v48
	v_mul_f32_e32 v7, 0xbcb8aa3b, v49
	v_exp_f32_e32 v10, v10
	v_exp_f32_e32 v11, v11
	v_exp_f32_e32 v6, v6
	v_exp_f32_e32 v7, v7
	v_add_f32_e32 v4, 1.0, v10
	v_add_f32_e32 v5, 1.0, v11
	v_add_f32_e32 v6, 1.0, v6
	v_add_f32_e32 v7, 1.0, v7
	v_rcp_f32_e32 v4, v4
	v_rcp_f32_e32 v5, v5
	v_rcp_f32_e32 v6, v6
	v_rcp_f32_e32 v7, v7
	v_fmamk_f32 v4, v4, 0x437f0000, v196
	v_fmamk_f32 v5, v5, 0x437f0000, v196
	v_fmamk_f32 v6, v6, 0x437f0000, v196
	v_fmamk_f32 v7, v7, 0x437f0000, v196
	v_perm_b32 v4, v5, v4, s67
	v_perm_b32 v5, v7, v6, s67
	v_mul_f32_e32 v6, 0xbcb8aa3b, v42
	v_mul_f32_e32 v7, 0xbcb8aa3b, v43
	v_exp_f32_e32 v6, v6
	v_exp_f32_e32 v7, v7
	v_perm_b32 v4, v5, v4, s68
	v_add_f32_e32 v5, 1.0, v6
	v_add_f32_e32 v6, 1.0, v7
	v_mul_f32_e32 v7, 0xbcb8aa3b, v44
	v_mul_f32_e32 v8, 0xbcb8aa3b, v45
	v_exp_f32_e32 v7, v7
	v_exp_f32_e32 v8, v8
	v_rcp_f32_e32 v5, v5
	v_rcp_f32_e32 v6, v6
	v_add_f32_e32 v7, 1.0, v7
	v_add_f32_e32 v8, 1.0, v8
	v_rcp_f32_e32 v7, v7
	v_rcp_f32_e32 v8, v8
	v_fmamk_f32 v5, v5, 0x437f0000, v196
	v_fmamk_f32 v6, v6, 0x437f0000, v196
	v_fmamk_f32 v7, v7, 0x437f0000, v196
	v_fmamk_f32 v8, v8, 0x437f0000, v196
	v_perm_b32 v5, v6, v5, s67
	v_perm_b32 v6, v8, v7, s67
	v_mul_f32_e32 v7, 0xbcb8aa3b, v38
	v_mul_f32_e32 v8, 0xbcb8aa3b, v39
	v_exp_f32_e32 v7, v7
	v_exp_f32_e32 v8, v8
	v_perm_b32 v5, v6, v5, s68
	v_add_f32_e32 v6, 1.0, v7
	v_add_f32_e32 v7, 1.0, v8
	v_mul_f32_e32 v8, 0xbcb8aa3b, v40
	v_mul_f32_e32 v9, 0xbcb8aa3b, v41
	v_exp_f32_e32 v8, v8
	v_exp_f32_e32 v9, v9
	v_rcp_f32_e32 v6, v6
	v_rcp_f32_e32 v7, v7
	v_add_f32_e32 v8, 1.0, v8
	v_add_f32_e32 v9, 1.0, v9
	v_rcp_f32_e32 v8, v8
	v_rcp_f32_e32 v9, v9
	v_fmamk_f32 v6, v6, 0x437f0000, v196
	v_fmamk_f32 v7, v7, 0x437f0000, v196
	v_fmamk_f32 v8, v8, 0x437f0000, v196
	v_fmamk_f32 v9, v9, 0x437f0000, v196
	v_perm_b32 v6, v7, v6, s67
	v_perm_b32 v7, v9, v8, s67
	v_mul_f32_e32 v8, 0xbcb8aa3b, v34
	v_mul_f32_e32 v9, 0xbcb8aa3b, v35
	v_exp_f32_e32 v8, v8
	v_exp_f32_e32 v9, v9
	v_perm_b32 v6, v7, v6, s68
	v_add_f32_e32 v7, 1.0, v8
	v_add_f32_e32 v8, 1.0, v9
	v_mul_f32_e32 v9, 0xbcb8aa3b, v36
	v_mul_f32_e32 v10, 0xbcb8aa3b, v37
	v_exp_f32_e32 v9, v9
	v_exp_f32_e32 v10, v10
	v_rcp_f32_e32 v7, v7
	v_rcp_f32_e32 v8, v8
	v_add_f32_e32 v9, 1.0, v9
	v_add_f32_e32 v10, 1.0, v10
	v_rcp_f32_e32 v9, v9
	v_rcp_f32_e32 v10, v10
	v_fmamk_f32 v7, v7, 0x437f0000, v196
	v_fmamk_f32 v8, v8, 0x437f0000, v196
	v_fmamk_f32 v9, v9, 0x437f0000, v196
	v_fmamk_f32 v10, v10, 0x437f0000, v196
	v_add_co_u32_e32 v2, vcc, 0x58000, v2
	v_perm_b32 v7, v8, v7, s67
	v_perm_b32 v8, v10, v9, s67
	v_addc_co_u32_e32 v3, vcc, 0, v3, vcc
	v_perm_b32 v7, v8, v7, s68
	s_andn2_b64 vcc, exec, s[0:1]
	s_mov_b64 s[0:1], -1
	global_store_dwordx4 v[2:3], v[4:7], off
; __device__ __forceinline__ float fsigmoid(float x) { return __builtin_amdgcn_rcpf(1.0f + __builtin_amdgcn_exp2f(-1.44269504f * x)); }
; __device__ __forceinline__ unsigned pk4_u8(float a, float b, float c, float d) {
;     const unsigned ya = __builtin_bit_cast(unsigned, a * 255.0f + 8388608.0f), yb = __builtin_bit_cast(unsigned, b * 255.0f + 8388608.0f), yc = __builtin_bit_cast(unsigned, c * 255.0f + 8388608.0f), yd = __builtin_bit_cast(unsigned, d * 255.0f + 8388608.0f);
;     const unsigned w01 = __builtin_amdgcn_perm(yb, ya, 0x0c0c0400u), w23 = __builtin_amdgcn_perm(yd, yc, 0x0c0c0400u);
;     return __builtin_amdgcn_perm(w23, w01, 0x05040100u); }
;     __device__ __forceinline__ void operator()(AccRef acc, const GUnit& u, int wr, int wc, int fr, int fq) const {
;         const int pm = u.x0, pn = u.x1; unsigned char* base = (pn < 8 ? GZF : GZS) + (size_t)(pm * 256 + wr * 64 + fr) * D + (pn & 7) * 256 + wc * 64 + 16 * fq;
; #pragma unroll
;         for (int ai = 0; ai < 2; ++ai)
; #pragma unroll
;             for (int m = 0; m < 4; ++m) { u32x4 w;
; #pragma unroll
;                 for (int bj = 0; bj < 2; ++bj)
; #pragma unroll
;                     for (int n = 0; n < 2; ++n) { const f32x4 v = acc[ai][bj][m][n]; w[bj * 2 + n] = pk4_u8(fsigmoid(v[0] * W8_INV), fsigmoid(v[1] * W8_INV), fsigmoid(v[2] * W8_INV), fsigmoid(v[3] * W8_INV)); }
;                 *(u32x4*)(base + (size_t)(ai * 128 + m * 16) * D) = w; }
.Lwtj_g:
	s_cbranch_vccnz .LBB0_420
	s_andn2_b64 vcc, exec, s[10:11]
	s_cbranch_vccnz .LBB0_419
	s_branch .LBB0_419
.Lwt_g:
	s_nop 15
	s_nop 7
	v_lshl_add_u32 v2, s8, 8, v190
	v_mul_f32_e32 v4, 0xbcb8aa3b, v158
	v_mul_f32_e32 v5, 0xbcb8aa3b, v159
	v_mul_f32_e32 v6, 0xbcb8aa3b, v160
	v_mul_f32_e32 v7, 0xbcb8aa3b, v161
	v_exp_f32_e32 v4, v4
	v_exp_f32_e32 v5, v5
	v_exp_f32_e32 v6, v6
	v_exp_f32_e32 v7, v7
	v_add_f32_e32 v4, 1.0, v4
	v_add_f32_e32 v5, 1.0, v5
	v_add_f32_e32 v6, 1.0, v6
	v_add_f32_e32 v7, 1.0, v7
	v_rcp_f32_e32 v4, v4
	v_rcp_f32_e32 v5, v5
	v_rcp_f32_e32 v6, v6
	v_rcp_f32_e32 v7, v7
	v_fmamk_f32 v4, v4, 0x437f0000, v196
	v_fmamk_f32 v5, v5, 0x437f0000, v196
	v_fmamk_f32 v6, v6, 0x437f0000, v196
	v_fmamk_f32 v7, v7, 0x437f0000, v196
	v_perm_b32 v4, v5, v4, s67
	v_perm_b32 v5, v7, v6, s67
	v_mul_f32_e32 v6, 0xbcb8aa3b, v154
	v_mul_f32_e32 v7, 0xbcb8aa3b, v155
	v_exp_f32_e32 v6, v6
	v_exp_f32_e32 v7, v7
	v_perm_b32 v4, v5, v4, s68
	v_add_f32_e32 v5, 1.0, v6
	v_add_f32_e32 v6, 1.0, v7
	v_mul_f32_e32 v7, 0xbcb8aa3b, v156
	v_mul_f32_e32 v8, 0xbcb8aa3b, v157
	v_exp_f32_e32 v7, v7
	v_exp_f32_e32 v8, v8
	v_rcp_f32_e32 v5, v5
	v_rcp_f32_e32 v6, v6
	v_add_f32_e32 v7, 1.0, v7
	v_add_f32_e32 v8, 1.0, v8
	v_rcp_f32_e32 v7, v7
	v_rcp_f32_e32 v8, v8
	v_fmamk_f32 v5, v5, 0x437f0000, v196
	v_fmamk_f32 v6, v6, 0x437f0000, v196
	v_fmamk_f32 v7, v7, 0x437f0000, v196
	v_fmamk_f32 v8, v8, 0x437f0000, v196
	v_perm_b32 v5, v6, v5, s67
	v_perm_b32 v6, v8, v7, s67
	v_mul_f32_e32 v7, 0xbcb8aa3b, v150
	v_mul_f32_e32 v8, 0xbcb8aa3b, v151
	v_exp_f32_e32 v7, v7
	v_exp_f32_e32 v8, v8
	v_perm_b32 v5, v6, v5, s68
	v_add_f32_e32 v6, 1.0, v7
	v_add_f32_e32 v7, 1.0, v8
	v_mul_f32_e32 v8, 0xbcb8aa3b, v152
	v_mul_f32_e32 v9, 0xbcb8aa3b, v153
	v_exp_f32_e32 v8, v8
	v_exp_f32_e32 v9, v9
	v_rcp_f32_e32 v6, v6
	v_rcp_f32_e32 v7, v7
	v_add_f32_e32 v8, 1.0, v8
	v_add_f32_e32 v9, 1.0, v9
	v_rcp_f32_e32 v8, v8
	v_rcp_f32_e32 v9, v9
	v_fmamk_f32 v6, v6, 0x437f0000, v196
	v_fmamk_f32 v7, v7, 0x437f0000, v196
	v_fmamk_f32 v8, v8, 0x437f0000, v196
	v_fmamk_f32 v9, v9, 0x437f0000, v196
	v_perm_b32 v6, v7, v6, s67
	v_perm_b32 v7, v9, v8, s67
	v_mul_f32_e32 v8, 0xbcb8aa3b, v146
	v_mul_f32_e32 v9, 0xbcb8aa3b, v147
	v_exp_f32_e32 v8, v8
	v_exp_f32_e32 v9, v9
	v_perm_b32 v6, v7, v6, s68
	v_add_f32_e32 v7, 1.0, v8
	v_add_f32_e32 v8, 1.0, v9
	v_mul_f32_e32 v9, 0xbcb8aa3b, v148
	v_mul_f32_e32 v10, 0xbcb8aa3b, v149
	v_exp_f32_e32 v9, v9
	v_exp_f32_e32 v10, v10
	v_rcp_f32_e32 v7, v7
	v_rcp_f32_e32 v8, v8
	v_add_f32_e32 v9, 1.0, v9
	v_add_f32_e32 v10, 1.0, v10
	v_rcp_f32_e32 v9, v9
	v_rcp_f32_e32 v10, v10
	s_cmp_lt_i32 s73, 8
	v_ashrrev_i32_e32 v3, 31, v2
	s_cselect_b32 s25, s41, s59
	s_cselect_b32 s24, s40, s53
	v_lshlrev_b64 v[2:3], 11, v[2:3]
	s_lshl_b32 s8, s73, 8
	v_lshl_add_u64 v[2:3], s[24:25], 0, v[2:3]
	s_and_b32 s8, s8, 0x700
	v_lshl_add_u64 v[2:3], v[2:3], 0, s[8:9]
	v_fmamk_f32 v7, v7, 0x437f0000, v196
	v_fmamk_f32 v8, v8, 0x437f0000, v196
	v_fmamk_f32 v9, v9, 0x437f0000, v196
	v_fmamk_f32 v10, v10, 0x437f0000, v196
	v_lshl_add_u64 v[2:3], v[2:3], 0, s[14:15]
	v_perm_b32 v7, v8, v7, s67
	v_perm_b32 v8, v10, v9, s67
	v_lshl_add_u64 v[2:3], v[2:3], 0, v[162:163]
	v_perm_b32 v7, v8, v7, s68
	global_store_dwordx4 v[2:3], v[4:7], off sc1
	v_mul_f32_e32 v8, 0xbcb8aa3b, v142
	v_mul_f32_e32 v9, 0xbcb8aa3b, v143
	v_mul_f32_e32 v6, 0xbcb8aa3b, v144
	v_mul_f32_e32 v7, 0xbcb8aa3b, v145
	v_exp_f32_e32 v8, v8
	v_exp_f32_e32 v9, v9
	v_exp_f32_e32 v6, v6
	v_exp_f32_e32 v7, v7
	v_add_f32_e32 v4, 1.0, v8
	v_add_f32_e32 v5, 1.0, v9
	v_add_f32_e32 v6, 1.0, v6
	v_add_f32_e32 v7, 1.0, v7
	v_rcp_f32_e32 v4, v4
	v_rcp_f32_e32 v5, v5
	v_rcp_f32_e32 v6, v6
	v_rcp_f32_e32 v7, v7
	v_fmamk_f32 v4, v4, 0x437f0000, v196
	v_fmamk_f32 v5, v5, 0x437f0000, v196
	v_fmamk_f32 v6, v6, 0x437f0000, v196
	v_fmamk_f32 v7, v7, 0x437f0000, v196
	v_perm_b32 v4, v5, v4, s67
	v_perm_b32 v5, v7, v6, s67
	v_mul_f32_e32 v6, 0xbcb8aa3b, v138
	v_mul_f32_e32 v7, 0xbcb8aa3b, v139
	v_exp_f32_e32 v6, v6
	v_exp_f32_e32 v7, v7
	v_perm_b32 v4, v5, v4, s68
	v_add_f32_e32 v5, 1.0, v6
	v_add_f32_e32 v6, 1.0, v7
	v_mul_f32_e32 v7, 0xbcb8aa3b, v140
	v_mul_f32_e32 v8, 0xbcb8aa3b, v141
	v_exp_f32_e32 v7, v7
	v_exp_f32_e32 v8, v8
	v_rcp_f32_e32 v5, v5
	v_rcp_f32_e32 v6, v6
	v_add_f32_e32 v7, 1.0, v7
	v_add_f32_e32 v8, 1.0, v8
	v_rcp_f32_e32 v7, v7
	v_rcp_f32_e32 v8, v8
	v_fmamk_f32 v5, v5, 0x437f0000, v196
	v_fmamk_f32 v6, v6, 0x437f0000, v196
	v_fmamk_f32 v7, v7, 0x437f0000, v196
	v_fmamk_f32 v8, v8, 0x437f0000, v196
	v_perm_b32 v5, v6, v5, s67
	v_perm_b32 v6, v8, v7, s67
	v_mul_f32_e32 v7, 0xbcb8aa3b, v134
	v_mul_f32_e32 v8, 0xbcb8aa3b, v135
	v_exp_f32_e32 v7, v7
	v_exp_f32_e32 v8, v8
	v_perm_b32 v5, v6, v5, s68
	v_add_f32_e32 v6, 1.0, v7
	v_add_f32_e32 v7, 1.0, v8
	v_mul_f32_e32 v8, 0xbcb8aa3b, v136
	v_mul_f32_e32 v9, 0xbcb8aa3b, v137
	v_exp_f32_e32 v8, v8
	v_exp_f32_e32 v9, v9
	v_rcp_f32_e32 v6, v6
	v_rcp_f32_e32 v7, v7
	v_add_f32_e32 v8, 1.0, v8
	v_add_f32_e32 v9, 1.0, v9
	v_rcp_f32_e32 v8, v8
	v_rcp_f32_e32 v9, v9
	v_fmamk_f32 v6, v6, 0x437f0000, v196
	v_fmamk_f32 v7, v7, 0x437f0000, v196
	v_fmamk_f32 v8, v8, 0x437f0000, v196
	v_fmamk_f32 v9, v9, 0x437f0000, v196
	v_perm_b32 v6, v7, v6, s67
	v_perm_b32 v7, v9, v8, s67
	v_mul_f32_e32 v8, 0xbcb8aa3b, v130
	v_mul_f32_e32 v9, 0xbcb8aa3b, v131
	v_exp_f32_e32 v8, v8
	v_exp_f32_e32 v9, v9
	v_perm_b32 v6, v7, v6, s68
	v_add_f32_e32 v7, 1.0, v8
	v_add_f32_e32 v8, 1.0, v9
	v_mul_f32_e32 v9, 0xbcb8aa3b, v132
	v_mul_f32_e32 v10, 0xbcb8aa3b, v133
	v_exp_f32_e32 v9, v9
	v_exp_f32_e32 v10, v10
	v_rcp_f32_e32 v7, v7
	v_rcp_f32_e32 v8, v8
	v_add_f32_e32 v9, 1.0, v9
	v_add_f32_e32 v10, 1.0, v10
; __device__ __forceinline__ float fsigmoid(float x) { return __builtin_amdgcn_rcpf(1.0f + __builtin_amdgcn_exp2f(-1.44269504f * x)); }
; __device__ __forceinline__ unsigned pk4_u8(float a, float b, float c, float d) {
;     const unsigned ya = __builtin_bit_cast(unsigned, a * 255.0f + 8388608.0f), yb = __builtin_bit_cast(unsigned, b * 255.0f + 8388608.0f), yc = __builtin_bit_cast(unsigned, c * 255.0f + 8388608.0f), yd = __builtin_bit_cast(unsigned, d * 255.0f + 8388608.0f);
;     const unsigned w01 = __builtin_amdgcn_perm(yb, ya, 0x0c0c0400u), w23 = __builtin_amdgcn_perm(yd, yc, 0x0c0c0400u);
;     return __builtin_amdgcn_perm(w23, w01, 0x05040100u); }
;     __device__ __forceinline__ void operator()(AccRef acc, const GUnit& u, int wr, int wc, int fr, int fq) const {
;     ...
;             for (int m = 0; m < 4; ++m) { u32x4 w;
; #pragma unroll
;                 for (int bj = 0; bj < 2; ++bj)
; #pragma unroll
;                     for (int n = 0; n < 2; ++n) { const f32x4 v = acc[ai][bj][m][n]; w[bj * 2 + n] = pk4_u8(fsigmoid(v[0] * W8_INV), fsigmoid(v[1] * W8_INV), fsigmoid(v[2] * W8_INV), fsigmoid(v[3] * W8_INV)); }
;                 *(u32x4*)(base + (size_t)(ai * 128 + m * 16) * D) = w; }
	v_rcp_f32_e32 v9, v9
	v_rcp_f32_e32 v10, v10
	v_fmamk_f32 v7, v7, 0x437f0000, v196
	v_fmamk_f32 v8, v8, 0x437f0000, v196
	v_fmamk_f32 v9, v9, 0x437f0000, v196
	v_fmamk_f32 v10, v10, 0x437f0000, v196
	v_perm_b32 v7, v8, v7, s67
	v_perm_b32 v8, v10, v9, s67
	v_perm_b32 v7, v8, v7, s68
	v_add_co_u32_e32 v8, vcc, s63, v2
	s_nop 0
	s_nop 0
	v_addc_co_u32_e32 v9, vcc, 0, v3, vcc
	global_store_dwordx4 v[8:9], v[4:7], off sc1
	v_mul_f32_e32 v10, 0xbcb8aa3b, v126
	v_mul_f32_e32 v11, 0xbcb8aa3b, v127
	v_mul_f32_e32 v6, 0xbcb8aa3b, v128
	v_mul_f32_e32 v7, 0xbcb8aa3b, v129
	v_exp_f32_e32 v10, v10
	v_exp_f32_e32 v11, v11
	v_exp_f32_e32 v6, v6
	v_exp_f32_e32 v7, v7
	v_add_f32_e32 v4, 1.0, v10
	v_add_f32_e32 v5, 1.0, v11
	v_add_f32_e32 v6, 1.0, v6
	v_add_f32_e32 v7, 1.0, v7
	v_rcp_f32_e32 v4, v4
	v_rcp_f32_e32 v5, v5
	v_rcp_f32_e32 v6, v6
	v_rcp_f32_e32 v7, v7
	v_fmamk_f32 v4, v4, 0x437f0000, v196
	v_fmamk_f32 v5, v5, 0x437f0000, v196
	v_fmamk_f32 v6, v6, 0x437f0000, v196
	v_fmamk_f32 v7, v7, 0x437f0000, v196
	v_perm_b32 v4, v5, v4, s67
	v_perm_b32 v5, v7, v6, s67
	v_mul_f32_e32 v6, 0xbcb8aa3b, v122
	v_mul_f32_e32 v7, 0xbcb8aa3b, v123
	v_exp_f32_e32 v6, v6
	v_exp_f32_e32 v7, v7
	v_perm_b32 v4, v5, v4, s68
	v_add_f32_e32 v5, 1.0, v6
	v_add_f32_e32 v6, 1.0, v7
	v_mul_f32_e32 v7, 0xbcb8aa3b, v124
	v_mul_f32_e32 v8, 0xbcb8aa3b, v125
	v_exp_f32_e32 v7, v7
	v_exp_f32_e32 v8, v8
	v_rcp_f32_e32 v5, v5
	v_rcp_f32_e32 v6, v6
	v_add_f32_e32 v7, 1.0, v7
	v_add_f32_e32 v8, 1.0, v8
	v_rcp_f32_e32 v7, v7
	v_rcp_f32_e32 v8, v8
	v_fmamk_f32 v5, v5, 0x437f0000, v196
	v_fmamk_f32 v6, v6, 0x437f0000, v196
	v_fmamk_f32 v7, v7, 0x437f0000, v196
	v_fmamk_f32 v8, v8, 0x437f0000, v196
	v_perm_b32 v5, v6, v5, s67
	v_perm_b32 v6, v8, v7, s67
	v_mul_f32_e32 v7, 0xbcb8aa3b, v118
	v_mul_f32_e32 v8, 0xbcb8aa3b, v119
	v_exp_f32_e32 v7, v7
	v_exp_f32_e32 v8, v8
	v_perm_b32 v5, v6, v5, s68
	v_add_f32_e32 v6, 1.0, v7
	v_add_f32_e32 v7, 1.0, v8
	v_mul_f32_e32 v8, 0xbcb8aa3b, v120
	v_mul_f32_e32 v9, 0xbcb8aa3b, v121
	v_exp_f32_e32 v8, v8
	v_exp_f32_e32 v9, v9
	v_rcp_f32_e32 v6, v6
	v_rcp_f32_e32 v7, v7
	v_add_f32_e32 v8, 1.0, v8
	v_add_f32_e32 v9, 1.0, v9
	v_rcp_f32_e32 v8, v8
	v_rcp_f32_e32 v9, v9
	v_fmamk_f32 v6, v6, 0x437f0000, v196
	v_fmamk_f32 v7, v7, 0x437f0000, v196
	v_fmamk_f32 v8, v8, 0x437f0000, v196
	v_fmamk_f32 v9, v9, 0x437f0000, v196
	v_perm_b32 v6, v7, v6, s67
	v_perm_b32 v7, v9, v8, s67
	v_mul_f32_e32 v8, 0xbcb8aa3b, v114
	v_mul_f32_e32 v9, 0xbcb8aa3b, v115
	v_exp_f32_e32 v8, v8
	v_exp_f32_e32 v9, v9
	v_perm_b32 v6, v7, v6, s68
	v_add_f32_e32 v7, 1.0, v8
	v_add_f32_e32 v8, 1.0, v9
	v_mul_f32_e32 v9, 0xbcb8aa3b, v116
	v_mul_f32_e32 v10, 0xbcb8aa3b, v117
	v_exp_f32_e32 v9, v9
	v_exp_f32_e32 v10, v10
	v_rcp_f32_e32 v7, v7
	v_rcp_f32_e32 v8, v8
	v_add_f32_e32 v9, 1.0, v9
	v_add_f32_e32 v10, 1.0, v10
	v_rcp_f32_e32 v9, v9
	v_rcp_f32_e32 v10, v10
	v_fmamk_f32 v7, v7, 0x437f0000, v196
	v_fmamk_f32 v8, v8, 0x437f0000, v196
	v_fmamk_f32 v9, v9, 0x437f0000, v196
	v_fmamk_f32 v10, v10, 0x437f0000, v196
	v_perm_b32 v7, v8, v7, s67
	v_perm_b32 v8, v10, v9, s67
	v_perm_b32 v7, v8, v7, s68
	v_add_co_u32_e32 v8, vcc, s52, v2
	s_nop 0
	s_nop 0
	v_addc_co_u32_e32 v9, vcc, 0, v3, vcc
	global_store_dwordx4 v[8:9], v[4:7], off sc1
	v_mul_f32_e32 v10, 0xbcb8aa3b, v110
	v_mul_f32_e32 v11, 0xbcb8aa3b, v111
	v_mul_f32_e32 v6, 0xbcb8aa3b, v112
	v_mul_f32_e32 v7, 0xbcb8aa3b, v113
	v_exp_f32_e32 v10, v10
	v_exp_f32_e32 v11, v11
	v_exp_f32_e32 v6, v6
	v_exp_f32_e32 v7, v7
	v_add_f32_e32 v4, 1.0, v10
	v_add_f32_e32 v5, 1.0, v11
	v_add_f32_e32 v6, 1.0, v6
	v_add_f32_e32 v7, 1.0, v7
	v_rcp_f32_e32 v4, v4
	v_rcp_f32_e32 v5, v5
	v_rcp_f32_e32 v6, v6
	v_rcp_f32_e32 v7, v7
	v_fmamk_f32 v4, v4, 0x437f0000, v196
	v_fmamk_f32 v5, v5, 0x437f0000, v196
	v_fmamk_f32 v6, v6, 0x437f0000, v196
	v_fmamk_f32 v7, v7, 0x437f0000, v196
	v_perm_b32 v4, v5, v4, s67
	v_perm_b32 v5, v7, v6, s67
	v_mul_f32_e32 v6, 0xbcb8aa3b, v106
	v_mul_f32_e32 v7, 0xbcb8aa3b, v107
	v_exp_f32_e32 v6, v6
	v_exp_f32_e32 v7, v7
	v_perm_b32 v4, v5, v4, s68
	v_add_f32_e32 v5, 1.0, v6
	v_add_f32_e32 v6, 1.0, v7
	v_mul_f32_e32 v7, 0xbcb8aa3b, v108
	v_mul_f32_e32 v8, 0xbcb8aa3b, v109
	v_exp_f32_e32 v7, v7
	v_exp_f32_e32 v8, v8
	v_rcp_f32_e32 v5, v5
	v_rcp_f32_e32 v6, v6
	v_add_f32_e32 v7, 1.0, v7
	v_add_f32_e32 v8, 1.0, v8
	v_rcp_f32_e32 v7, v7
	v_rcp_f32_e32 v8, v8
	v_fmamk_f32 v5, v5, 0x437f0000, v196
	v_fmamk_f32 v6, v6, 0x437f0000, v196
	v_fmamk_f32 v7, v7, 0x437f0000, v196
	v_fmamk_f32 v8, v8, 0x437f0000, v196
	v_perm_b32 v5, v6, v5, s67
	v_perm_b32 v6, v8, v7, s67
	v_mul_f32_e32 v7, 0xbcb8aa3b, v102
	v_mul_f32_e32 v8, 0xbcb8aa3b, v103
	v_exp_f32_e32 v7, v7
	v_exp_f32_e32 v8, v8
	v_perm_b32 v5, v6, v5, s68
	v_add_f32_e32 v6, 1.0, v7
	v_add_f32_e32 v7, 1.0, v8
	v_mul_f32_e32 v8, 0xbcb8aa3b, v104
	v_mul_f32_e32 v9, 0xbcb8aa3b, v105
	v_exp_f32_e32 v8, v8
	v_exp_f32_e32 v9, v9
	v_rcp_f32_e32 v6, v6
	v_rcp_f32_e32 v7, v7
	v_add_f32_e32 v8, 1.0, v8
	v_add_f32_e32 v9, 1.0, v9
	v_rcp_f32_e32 v8, v8
	v_rcp_f32_e32 v9, v9
	v_fmamk_f32 v6, v6, 0x437f0000, v196
	v_fmamk_f32 v7, v7, 0x437f0000, v196
	v_fmamk_f32 v8, v8, 0x437f0000, v196
	v_fmamk_f32 v9, v9, 0x437f0000, v196
	v_perm_b32 v6, v7, v6, s67
	v_perm_b32 v7, v9, v8, s67
	v_mul_f32_e32 v8, 0xbcb8aa3b, v98
	v_mul_f32_e32 v9, 0xbcb8aa3b, v99
	v_exp_f32_e32 v8, v8
	v_exp_f32_e32 v9, v9
	v_perm_b32 v6, v7, v6, s68
	v_add_f32_e32 v7, 1.0, v8
	v_add_f32_e32 v8, 1.0, v9
	v_mul_f32_e32 v9, 0xbcb8aa3b, v100
	v_mul_f32_e32 v10, 0xbcb8aa3b, v101
	v_exp_f32_e32 v9, v9
	v_exp_f32_e32 v10, v10
	v_rcp_f32_e32 v7, v7
	v_rcp_f32_e32 v8, v8
	v_add_f32_e32 v9, 1.0, v9
	v_add_f32_e32 v10, 1.0, v10
	v_rcp_f32_e32 v9, v9
; __device__ __forceinline__ float fsigmoid(float x) { return __builtin_amdgcn_rcpf(1.0f + __builtin_amdgcn_exp2f(-1.44269504f * x)); }
; __device__ __forceinline__ unsigned pk4_u8(float a, float b, float c, float d) {
;     const unsigned ya = __builtin_bit_cast(unsigned, a * 255.0f + 8388608.0f), yb = __builtin_bit_cast(unsigned, b * 255.0f + 8388608.0f), yc = __builtin_bit_cast(unsigned, c * 255.0f + 8388608.0f), yd = __builtin_bit_cast(unsigned, d * 255.0f + 8388608.0f);
;     const unsigned w01 = __builtin_amdgcn_perm(yb, ya, 0x0c0c0400u), w23 = __builtin_amdgcn_perm(yd, yc, 0x0c0c0400u);
;     return __builtin_amdgcn_perm(w23, w01, 0x05040100u); }
;     __device__ __forceinline__ void operator()(AccRef acc, const GUnit& u, int wr, int wc, int fr, int fq) const {
;     ...
;             for (int m = 0; m < 4; ++m) { u32x4 w;
; #pragma unroll
;                 for (int bj = 0; bj < 2; ++bj)
; #pragma unroll
;                     for (int n = 0; n < 2; ++n) { const f32x4 v = acc[ai][bj][m][n]; w[bj * 2 + n] = pk4_u8(fsigmoid(v[0] * W8_INV), fsigmoid(v[1] * W8_INV), fsigmoid(v[2] * W8_INV), fsigmoid(v[3] * W8_INV)); }
;                 *(u32x4*)(base + (size_t)(ai * 128 + m * 16) * D) = w; }
	v_rcp_f32_e32 v10, v10
	v_fmamk_f32 v7, v7, 0x437f0000, v196
	v_fmamk_f32 v8, v8, 0x437f0000, v196
	v_fmamk_f32 v9, v9, 0x437f0000, v196
	v_fmamk_f32 v10, v10, 0x437f0000, v196
	v_perm_b32 v7, v8, v7, s67
	v_perm_b32 v8, v10, v9, s67
	v_perm_b32 v7, v8, v7, s68
	v_add_co_u32_e32 v8, vcc, s62, v2
	s_nop 0
	s_nop 0
	v_addc_co_u32_e32 v9, vcc, 0, v3, vcc
	global_store_dwordx4 v[8:9], v[4:7], off sc1
	v_mul_f32_e32 v10, 0xbcb8aa3b, v94
	v_mul_f32_e32 v11, 0xbcb8aa3b, v95
	v_mul_f32_e32 v6, 0xbcb8aa3b, v96
	v_mul_f32_e32 v7, 0xbcb8aa3b, v97
	v_exp_f32_e32 v10, v10
	v_exp_f32_e32 v11, v11
	v_exp_f32_e32 v6, v6
	v_exp_f32_e32 v7, v7
	v_add_f32_e32 v4, 1.0, v10
	v_add_f32_e32 v5, 1.0, v11
	v_add_f32_e32 v6, 1.0, v6
	v_add_f32_e32 v7, 1.0, v7
	v_rcp_f32_e32 v4, v4
	v_rcp_f32_e32 v5, v5
	v_rcp_f32_e32 v6, v6
	v_rcp_f32_e32 v7, v7
	v_fmamk_f32 v4, v4, 0x437f0000, v196
	v_fmamk_f32 v5, v5, 0x437f0000, v196
	v_fmamk_f32 v6, v6, 0x437f0000, v196
	v_fmamk_f32 v7, v7, 0x437f0000, v196
	v_perm_b32 v4, v5, v4, s67
	v_perm_b32 v5, v7, v6, s67
	v_mul_f32_e32 v6, 0xbcb8aa3b, v90
	v_mul_f32_e32 v7, 0xbcb8aa3b, v91
	v_exp_f32_e32 v6, v6
	v_exp_f32_e32 v7, v7
	v_perm_b32 v4, v5, v4, s68
	v_add_f32_e32 v5, 1.0, v6
	v_add_f32_e32 v6, 1.0, v7
	v_mul_f32_e32 v7, 0xbcb8aa3b, v92
	v_mul_f32_e32 v8, 0xbcb8aa3b, v93
	v_exp_f32_e32 v7, v7
	v_exp_f32_e32 v8, v8
	v_rcp_f32_e32 v5, v5
	v_rcp_f32_e32 v6, v6
	v_add_f32_e32 v7, 1.0, v7
	v_add_f32_e32 v8, 1.0, v8
	v_rcp_f32_e32 v7, v7
	v_rcp_f32_e32 v8, v8
	v_fmamk_f32 v5, v5, 0x437f0000, v196
	v_fmamk_f32 v6, v6, 0x437f0000, v196
	v_fmamk_f32 v7, v7, 0x437f0000, v196
	v_fmamk_f32 v8, v8, 0x437f0000, v196
	v_perm_b32 v5, v6, v5, s67
	v_perm_b32 v6, v8, v7, s67
	v_mul_f32_e32 v7, 0xbcb8aa3b, v86
	v_mul_f32_e32 v8, 0xbcb8aa3b, v87
	v_exp_f32_e32 v7, v7
	v_exp_f32_e32 v8, v8
	v_perm_b32 v5, v6, v5, s68
	v_add_f32_e32 v6, 1.0, v7
	v_add_f32_e32 v7, 1.0, v8
	v_mul_f32_e32 v8, 0xbcb8aa3b, v88
	v_mul_f32_e32 v9, 0xbcb8aa3b, v89
	v_exp_f32_e32 v8, v8
	v_exp_f32_e32 v9, v9
	v_rcp_f32_e32 v6, v6
	v_rcp_f32_e32 v7, v7
	v_add_f32_e32 v8, 1.0, v8
	v_add_f32_e32 v9, 1.0, v9
	v_rcp_f32_e32 v8, v8
	v_rcp_f32_e32 v9, v9
	v_fmamk_f32 v6, v6, 0x437f0000, v196
	v_fmamk_f32 v7, v7, 0x437f0000, v196
	v_fmamk_f32 v8, v8, 0x437f0000, v196
	v_fmamk_f32 v9, v9, 0x437f0000, v196
	v_perm_b32 v6, v7, v6, s67
	v_perm_b32 v7, v9, v8, s67
	v_mul_f32_e32 v8, 0xbcb8aa3b, v82
	v_mul_f32_e32 v9, 0xbcb8aa3b, v83
	v_exp_f32_e32 v8, v8
	v_exp_f32_e32 v9, v9
	v_perm_b32 v6, v7, v6, s68
	v_add_f32_e32 v7, 1.0, v8
	v_add_f32_e32 v8, 1.0, v9
	v_mul_f32_e32 v9, 0xbcb8aa3b, v84
	v_mul_f32_e32 v10, 0xbcb8aa3b, v85
	v_exp_f32_e32 v9, v9
	v_exp_f32_e32 v10, v10
	v_rcp_f32_e32 v7, v7
	v_rcp_f32_e32 v8, v8
	v_add_f32_e32 v9, 1.0, v9
	v_add_f32_e32 v10, 1.0, v10
	v_rcp_f32_e32 v9, v9
	v_rcp_f32_e32 v10, v10
	v_fmamk_f32 v7, v7, 0x437f0000, v196
	v_fmamk_f32 v8, v8, 0x437f0000, v196
	v_fmamk_f32 v9, v9, 0x437f0000, v196
	v_fmamk_f32 v10, v10, 0x437f0000, v196
	v_perm_b32 v7, v8, v7, s67
	v_perm_b32 v8, v10, v9, s67
	v_perm_b32 v7, v8, v7, s68
	v_add_co_u32_e32 v8, vcc, s69, v2
	s_nop 0
	s_nop 0
	v_addc_co_u32_e32 v9, vcc, 0, v3, vcc
	global_store_dwordx4 v[8:9], v[4:7], off sc1
	v_mul_f32_e32 v10, 0xbcb8aa3b, v78
	v_mul_f32_e32 v11, 0xbcb8aa3b, v79
	v_mul_f32_e32 v6, 0xbcb8aa3b, v80
	v_mul_f32_e32 v7, 0xbcb8aa3b, v81
	v_exp_f32_e32 v10, v10
	v_exp_f32_e32 v11, v11
	v_exp_f32_e32 v6, v6
	v_exp_f32_e32 v7, v7
	v_add_f32_e32 v4, 1.0, v10
	v_add_f32_e32 v5, 1.0, v11
	v_add_f32_e32 v6, 1.0, v6
	v_add_f32_e32 v7, 1.0, v7
	v_rcp_f32_e32 v4, v4
	v_rcp_f32_e32 v5, v5
	v_rcp_f32_e32 v6, v6
	v_rcp_f32_e32 v7, v7
	v_fmamk_f32 v4, v4, 0x437f0000, v196
	v_fmamk_f32 v5, v5, 0x437f0000, v196
	v_fmamk_f32 v6, v6, 0x437f0000, v196
	v_fmamk_f32 v7, v7, 0x437f0000, v196
	v_perm_b32 v4, v5, v4, s67
	v_perm_b32 v5, v7, v6, s67
	v_mul_f32_e32 v6, 0xbcb8aa3b, v74
	v_mul_f32_e32 v7, 0xbcb8aa3b, v75
	v_exp_f32_e32 v6, v6
	v_exp_f32_e32 v7, v7
	v_perm_b32 v4, v5, v4, s68
	v_add_f32_e32 v5, 1.0, v6
	v_add_f32_e32 v6, 1.0, v7
	v_mul_f32_e32 v7, 0xbcb8aa3b, v76
	v_mul_f32_e32 v8, 0xbcb8aa3b, v77
	v_exp_f32_e32 v7, v7
	v_exp_f32_e32 v8, v8
	v_rcp_f32_e32 v5, v5
	v_rcp_f32_e32 v6, v6
	v_add_f32_e32 v7, 1.0, v7
	v_add_f32_e32 v8, 1.0, v8
	v_rcp_f32_e32 v7, v7
	v_rcp_f32_e32 v8, v8
	v_fmamk_f32 v5, v5, 0x437f0000, v196
	v_fmamk_f32 v6, v6, 0x437f0000, v196
	v_fmamk_f32 v7, v7, 0x437f0000, v196
	v_fmamk_f32 v8, v8, 0x437f0000, v196
	v_perm_b32 v5, v6, v5, s67
	v_perm_b32 v6, v8, v7, s67
	v_mul_f32_e32 v7, 0xbcb8aa3b, v70
	v_mul_f32_e32 v8, 0xbcb8aa3b, v71
	v_exp_f32_e32 v7, v7
	v_exp_f32_e32 v8, v8
	v_perm_b32 v5, v6, v5, s68
	v_add_f32_e32 v6, 1.0, v7
	v_add_f32_e32 v7, 1.0, v8
	v_mul_f32_e32 v8, 0xbcb8aa3b, v72
	v_mul_f32_e32 v9, 0xbcb8aa3b, v73
	v_exp_f32_e32 v8, v8
	v_exp_f32_e32 v9, v9
	v_rcp_f32_e32 v6, v6
	v_rcp_f32_e32 v7, v7
	v_add_f32_e32 v8, 1.0, v8
	v_add_f32_e32 v9, 1.0, v9
	v_rcp_f32_e32 v8, v8
	v_rcp_f32_e32 v9, v9
	v_fmamk_f32 v6, v6, 0x437f0000, v196
	v_fmamk_f32 v7, v7, 0x437f0000, v196
	v_fmamk_f32 v8, v8, 0x437f0000, v196
	v_fmamk_f32 v9, v9, 0x437f0000, v196
	v_perm_b32 v6, v7, v6, s67
	v_perm_b32 v7, v9, v8, s67
	v_mul_f32_e32 v8, 0xbcb8aa3b, v66
	v_mul_f32_e32 v9, 0xbcb8aa3b, v67
	v_exp_f32_e32 v8, v8
	v_exp_f32_e32 v9, v9
	v_perm_b32 v6, v7, v6, s68
	v_add_f32_e32 v7, 1.0, v8
	v_add_f32_e32 v8, 1.0, v9
	v_mul_f32_e32 v9, 0xbcb8aa3b, v68
	v_mul_f32_e32 v10, 0xbcb8aa3b, v69
	v_exp_f32_e32 v9, v9
	v_exp_f32_e32 v10, v10
	v_rcp_f32_e32 v7, v7
	v_rcp_f32_e32 v8, v8
	v_add_f32_e32 v9, 1.0, v9
	v_add_f32_e32 v10, 1.0, v10
	v_rcp_f32_e32 v9, v9
	v_rcp_f32_e32 v10, v10
	v_fmamk_f32 v7, v7, 0x437f0000, v196
; __device__ __forceinline__ float fsigmoid(float x) { return __builtin_amdgcn_rcpf(1.0f + __builtin_amdgcn_exp2f(-1.44269504f * x)); }
; __device__ __forceinline__ unsigned pk4_u8(float a, float b, float c, float d) {
;     const unsigned ya = __builtin_bit_cast(unsigned, a * 255.0f + 8388608.0f), yb = __builtin_bit_cast(unsigned, b * 255.0f + 8388608.0f), yc = __builtin_bit_cast(unsigned, c * 255.0f + 8388608.0f), yd = __builtin_bit_cast(unsigned, d * 255.0f + 8388608.0f);
;     const unsigned w01 = __builtin_amdgcn_perm(yb, ya, 0x0c0c0400u), w23 = __builtin_amdgcn_perm(yd, yc, 0x0c0c0400u);
;     return __builtin_amdgcn_perm(w23, w01, 0x05040100u); }
;     __device__ __forceinline__ void operator()(AccRef acc, const GUnit& u, int wr, int wc, int fr, int fq) const {
;     ...
;             for (int m = 0; m < 4; ++m) { u32x4 w;
; #pragma unroll
;                 for (int bj = 0; bj < 2; ++bj)
; #pragma unroll
;                     for (int n = 0; n < 2; ++n) { const f32x4 v = acc[ai][bj][m][n]; w[bj * 2 + n] = pk4_u8(fsigmoid(v[0] * W8_INV), fsigmoid(v[1] * W8_INV), fsigmoid(v[2] * W8_INV), fsigmoid(v[3] * W8_INV)); }
;                 *(u32x4*)(base + (size_t)(ai * 128 + m * 16) * D) = w; }
	v_fmamk_f32 v8, v8, 0x437f0000, v196
	v_fmamk_f32 v9, v9, 0x437f0000, v196
	v_fmamk_f32 v10, v10, 0x437f0000, v196
	v_perm_b32 v7, v8, v7, s67
	v_perm_b32 v8, v10, v9, s67
	v_perm_b32 v7, v8, v7, s68
	v_add_co_u32_e32 v8, vcc, s70, v2
	s_nop 0
	s_nop 0
	v_addc_co_u32_e32 v9, vcc, 0, v3, vcc
	global_store_dwordx4 v[8:9], v[4:7], off sc1
	v_mul_f32_e32 v10, 0xbcb8aa3b, v62
	v_mul_f32_e32 v11, 0xbcb8aa3b, v63
	v_mul_f32_e32 v6, 0xbcb8aa3b, v64
	v_mul_f32_e32 v7, 0xbcb8aa3b, v65
	v_exp_f32_e32 v10, v10
	v_exp_f32_e32 v11, v11
	v_exp_f32_e32 v6, v6
	v_exp_f32_e32 v7, v7
	v_add_f32_e32 v4, 1.0, v10
	v_add_f32_e32 v5, 1.0, v11
	v_add_f32_e32 v6, 1.0, v6
	v_add_f32_e32 v7, 1.0, v7
	v_rcp_f32_e32 v4, v4
	v_rcp_f32_e32 v5, v5
	v_rcp_f32_e32 v6, v6
	v_rcp_f32_e32 v7, v7
	v_fmamk_f32 v4, v4, 0x437f0000, v196
	v_fmamk_f32 v5, v5, 0x437f0000, v196
	v_fmamk_f32 v6, v6, 0x437f0000, v196
	v_fmamk_f32 v7, v7, 0x437f0000, v196
	v_perm_b32 v4, v5, v4, s67
	v_perm_b32 v5, v7, v6, s67
	v_mul_f32_e32 v6, 0xbcb8aa3b, v58
	v_mul_f32_e32 v7, 0xbcb8aa3b, v59
	v_exp_f32_e32 v6, v6
	v_exp_f32_e32 v7, v7
	v_perm_b32 v4, v5, v4, s68
	v_add_f32_e32 v5, 1.0, v6
	v_add_f32_e32 v6, 1.0, v7
	v_mul_f32_e32 v7, 0xbcb8aa3b, v60
	v_mul_f32_e32 v8, 0xbcb8aa3b, v61
	v_exp_f32_e32 v7, v7
	v_exp_f32_e32 v8, v8
	v_rcp_f32_e32 v5, v5
	v_rcp_f32_e32 v6, v6
	v_add_f32_e32 v7, 1.0, v7
	v_add_f32_e32 v8, 1.0, v8
	v_rcp_f32_e32 v7, v7
	v_rcp_f32_e32 v8, v8
	v_fmamk_f32 v5, v5, 0x437f0000, v196
	v_fmamk_f32 v6, v6, 0x437f0000, v196
	v_fmamk_f32 v7, v7, 0x437f0000, v196
	v_fmamk_f32 v8, v8, 0x437f0000, v196
	v_perm_b32 v5, v6, v5, s67
	v_perm_b32 v6, v8, v7, s67
	v_mul_f32_e32 v7, 0xbcb8aa3b, v54
	v_mul_f32_e32 v8, 0xbcb8aa3b, v55
	v_exp_f32_e32 v7, v7
	v_exp_f32_e32 v8, v8
	v_perm_b32 v5, v6, v5, s68
	v_add_f32_e32 v6, 1.0, v7
	v_add_f32_e32 v7, 1.0, v8
	v_mul_f32_e32 v8, 0xbcb8aa3b, v56
	v_mul_f32_e32 v9, 0xbcb8aa3b, v57
	v_exp_f32_e32 v8, v8
	v_exp_f32_e32 v9, v9
	v_rcp_f32_e32 v6, v6
	v_rcp_f32_e32 v7, v7
	v_add_f32_e32 v8, 1.0, v8
	v_add_f32_e32 v9, 1.0, v9
	v_rcp_f32_e32 v8, v8
	v_rcp_f32_e32 v9, v9
	v_fmamk_f32 v6, v6, 0x437f0000, v196
	v_fmamk_f32 v7, v7, 0x437f0000, v196
	v_fmamk_f32 v8, v8, 0x437f0000, v196
	v_fmamk_f32 v9, v9, 0x437f0000, v196
	v_perm_b32 v6, v7, v6, s67
	v_perm_b32 v7, v9, v8, s67
	v_mul_f32_e32 v8, 0xbcb8aa3b, v50
	v_mul_f32_e32 v9, 0xbcb8aa3b, v51
	v_exp_f32_e32 v8, v8
	v_exp_f32_e32 v9, v9
	v_perm_b32 v6, v7, v6, s68
	v_add_f32_e32 v7, 1.0, v8
	v_add_f32_e32 v8, 1.0, v9
	v_mul_f32_e32 v9, 0xbcb8aa3b, v52
	v_mul_f32_e32 v10, 0xbcb8aa3b, v53
	v_exp_f32_e32 v9, v9
	v_exp_f32_e32 v10, v10
	v_rcp_f32_e32 v7, v7
	v_rcp_f32_e32 v8, v8
	v_add_f32_e32 v9, 1.0, v9
	v_add_f32_e32 v10, 1.0, v10
	v_rcp_f32_e32 v9, v9
	v_rcp_f32_e32 v10, v10
	v_fmamk_f32 v7, v7, 0x437f0000, v196
	v_fmamk_f32 v8, v8, 0x437f0000, v196
	v_fmamk_f32 v9, v9, 0x437f0000, v196
	v_fmamk_f32 v10, v10, 0x437f0000, v196
	v_perm_b32 v7, v8, v7, s67
	v_perm_b32 v8, v10, v9, s67
	v_perm_b32 v7, v8, v7, s68
	v_add_co_u32_e32 v8, vcc, s71, v2
	s_nop 0
	s_nop 0
	v_addc_co_u32_e32 v9, vcc, 0, v3, vcc
	global_store_dwordx4 v[8:9], v[4:7], off sc1
	v_mul_f32_e32 v10, 0xbcb8aa3b, v46
	v_mul_f32_e32 v11, 0xbcb8aa3b, v47
	v_mul_f32_e32 v6, 0xbcb8aa3b, v48
	v_mul_f32_e32 v7, 0xbcb8aa3b, v49
	v_exp_f32_e32 v10, v10
	v_exp_f32_e32 v11, v11
	v_exp_f32_e32 v6, v6
	v_exp_f32_e32 v7, v7
	v_add_f32_e32 v4, 1.0, v10
	v_add_f32_e32 v5, 1.0, v11
	v_add_f32_e32 v6, 1.0, v6
	v_add_f32_e32 v7, 1.0, v7
	v_rcp_f32_e32 v4, v4
	v_rcp_f32_e32 v5, v5
	v_rcp_f32_e32 v6, v6
	v_rcp_f32_e32 v7, v7
	v_fmamk_f32 v4, v4, 0x437f0000, v196
	v_fmamk_f32 v5, v5, 0x437f0000, v196
	v_fmamk_f32 v6, v6, 0x437f0000, v196
	v_fmamk_f32 v7, v7, 0x437f0000, v196
	v_perm_b32 v4, v5, v4, s67
	v_perm_b32 v5, v7, v6, s67
	v_mul_f32_e32 v6, 0xbcb8aa3b, v42
	v_mul_f32_e32 v7, 0xbcb8aa3b, v43
	v_exp_f32_e32 v6, v6
	v_exp_f32_e32 v7, v7
	v_perm_b32 v4, v5, v4, s68
	v_add_f32_e32 v5, 1.0, v6
	v_add_f32_e32 v6, 1.0, v7
	v_mul_f32_e32 v7, 0xbcb8aa3b, v44
	v_mul_f32_e32 v8, 0xbcb8aa3b, v45
	v_exp_f32_e32 v7, v7
	v_exp_f32_e32 v8, v8
	v_rcp_f32_e32 v5, v5
	v_rcp_f32_e32 v6, v6
	v_add_f32_e32 v7, 1.0, v7
	v_add_f32_e32 v8, 1.0, v8
	v_rcp_f32_e32 v7, v7
	v_rcp_f32_e32 v8, v8
	v_fmamk_f32 v5, v5, 0x437f0000, v196
	v_fmamk_f32 v6, v6, 0x437f0000, v196
	v_fmamk_f32 v7, v7, 0x437f0000, v196
	v_fmamk_f32 v8, v8, 0x437f0000, v196
	v_perm_b32 v5, v6, v5, s67
	v_perm_b32 v6, v8, v7, s67
	v_mul_f32_e32 v7, 0xbcb8aa3b, v38
	v_mul_f32_e32 v8, 0xbcb8aa3b, v39
	v_exp_f32_e32 v7, v7
	v_exp_f32_e32 v8, v8
	v_perm_b32 v5, v6, v5, s68
	v_add_f32_e32 v6, 1.0, v7
	v_add_f32_e32 v7, 1.0, v8
	v_mul_f32_e32 v8, 0xbcb8aa3b, v40
	v_mul_f32_e32 v9, 0xbcb8aa3b, v41
	v_exp_f32_e32 v8, v8
	v_exp_f32_e32 v9, v9
	v_rcp_f32_e32 v6, v6
	v_rcp_f32_e32 v7, v7
	v_add_f32_e32 v8, 1.0, v8
	v_add_f32_e32 v9, 1.0, v9
	v_rcp_f32_e32 v8, v8
	v_rcp_f32_e32 v9, v9
	v_fmamk_f32 v6, v6, 0x437f0000, v196
	v_fmamk_f32 v7, v7, 0x437f0000, v196
	v_fmamk_f32 v8, v8, 0x437f0000, v196
	v_fmamk_f32 v9, v9, 0x437f0000, v196
	v_perm_b32 v6, v7, v6, s67
	v_perm_b32 v7, v9, v8, s67
	v_mul_f32_e32 v8, 0xbcb8aa3b, v34
	v_mul_f32_e32 v9, 0xbcb8aa3b, v35
	v_exp_f32_e32 v8, v8
	v_exp_f32_e32 v9, v9
	v_perm_b32 v6, v7, v6, s68
	v_add_f32_e32 v7, 1.0, v8
	v_add_f32_e32 v8, 1.0, v9
	v_mul_f32_e32 v9, 0xbcb8aa3b, v36
	v_mul_f32_e32 v10, 0xbcb8aa3b, v37
	v_exp_f32_e32 v9, v9
	v_exp_f32_e32 v10, v10
	v_rcp_f32_e32 v7, v7
	v_rcp_f32_e32 v8, v8
	v_add_f32_e32 v9, 1.0, v9
	v_add_f32_e32 v10, 1.0, v10
	v_rcp_f32_e32 v9, v9
	v_rcp_f32_e32 v10, v10
	v_fmamk_f32 v7, v7, 0x437f0000, v196
	v_fmamk_f32 v8, v8, 0x437f0000, v196
	v_fmamk_f32 v9, v9, 0x437f0000, v196
	v_fmamk_f32 v10, v10, 0x437f0000, v196
	v_add_co_u32_e32 v2, vcc, 0x58000, v2
	v_perm_b32 v7, v8, v7, s67
	v_perm_b32 v8, v10, v9, s67
	v_addc_co_u32_e32 v3, vcc, 0, v3, vcc
	v_perm_b32 v7, v8, v7, s68
	s_andn2_b64 vcc, exec, s[0:1]
	s_mov_b64 s[0:1], -1
	global_store_dwordx4 v[2:3], v[4:7], off sc1
	s_branch .Lwtj_g

; __device__ __forceinline__ unsigned pk4_fp8(float a, float b, float c, float d) { int w = 0; w = __builtin_amdgcn_cvt_pk_fp8_f32(clamp8(a), clamp8(b), w, false); w = __builtin_amdgcn_cvt_pk_fp8_f32(clamp8(c), clamp8(d), w, true); return (unsigned)w; }
; __device__ __forceinline__ float clamp8(float x) { return __builtin_amdgcn_fmed3f(x, -448.0f, 448.0f); }
;     __device__ __forceinline__ void operator()(AccRef acc, const GUnit& u, int wr, int wc, int fr, int fq) const {
;         const int pm = u.x0, pn = u.x1; const float* gate = modv + (size_t)(pm >> 5) * 12288 + 2 * D;
;         const int col0 = pn * 256 + wc * 64 + 16 * fq;
;         f32x4 gv[4];
; #pragma unroll
;         for (int q = 0; q < 4; ++q) gv[q] = *(const f32x4*)(gate + col0 + 4 * q) * (W8_INV * MG8_SCALE);
; #pragma unroll
;         for (int ai = 0; ai < 2; ++ai)
; #pragma unroll
;             for (int m = 0; m < 4; ++m) { u32x4 w;
; #pragma unroll
;                 for (int q = 0; q < 4; ++q) { const f32x4 v = acc[ai][q >> 1][m][q & 1] * gv[q]; w[q] = pk4_fp8(v[0], v[1], v[2], v[3]); }
;                 *(u32x4*)(MG + (size_t)(pm * 256 + ai * 128 + wr * 64 + m * 16 + fr) * D + col0) = w; }
.LBB0_914:
	s_cmp_eq_u64 s[0:1], 0
	s_cbranch_scc1 .Lwt_o
	s_ashr_i32 s19, s26, 5
	s_mul_hi_i32 s21, s19, 0xc000
	s_mul_i32 s19, s19, 0xc000
	s_add_u32 s28, s36, s19
	v_lshl_or_b32 v2, s64, 8, v190
	s_addc_u32 s29, s37, s21
	v_ashrrev_i32_e32 v3, 31, v2
	v_lshl_add_u64 v[4:5], v[2:3], 2, s[28:29]
	v_add_co_u32_e32 v6, vcc, s62, v4
	s_nop 15
	s_nop 7
	s_nop 1
	v_addc_co_u32_e32 v7, vcc, 0, v5, vcc
	global_load_dwordx4 v[6:9], v[6:7], off
	v_lshl_add_u64 v[4:5], v[4:5], 0, s[14:15]
	global_load_dwordx4 v[10:13], v[4:5], off offset:16
	global_load_dwordx4 v[22:25], v[4:5], off offset:32
	global_load_dwordx4 v[26:29], v[4:5], off offset:48
	v_lshl_add_u32 v4, s26, 8, v188
	v_ashrrev_i32_e32 v5, 31, v4
	v_mov_b32_e32 v30, 0
	v_lshlrev_b64 v[14:15], 11, v[4:5]
	v_lshl_add_u64 v[14:15], s[10:11], 0, v[14:15]
	v_lshl_add_u64 v[200:201], v[14:15], 0, v[2:3]
	v_mov_b32_e32 v199, 0
	v_mov_b32_e32 v196, 0
	v_mov_b32_e32 v197, 0
	v_mov_b32_e32 v198, 0
	v_mov_b32_e32 v31, 0
	v_mov_b32_e32 v32, 0
	v_mov_b32_e32 v33, 0
	s_andn2_b64 vcc, exec, s[0:1]
	s_mov_b64 s[0:1], -1
	s_waitcnt vmcnt(0) lgkmcnt(0)
	v_pk_mul_f32 v[16:17], v[10:11], s[16:17] op_sel_hi:[1,0]
	v_pk_mul_f32 v[20:21], v[6:7], s[16:17] op_sel_hi:[1,0]
	v_pk_mul_f32 v[10:11], v[24:25], s[16:17] op_sel_hi:[1,0]
	v_pk_mul_f32 v[24:25], v[158:159], v[20:21]
	v_pk_mul_f32 v[18:19], v[8:9], s[16:17] op_sel_hi:[1,0]
	v_med3_f32 v5, v24, s63, v195
	v_med3_f32 v24, v25, s63, v195
	v_cvt_pk_fp8_f32 v30, v5, v24
	v_pk_mul_f32 v[14:15], v[12:13], s[16:17] op_sel_hi:[1,0]
	v_pk_mul_f32 v[12:13], v[22:23], s[16:17] op_sel_hi:[1,0]
	v_pk_mul_f32 v[22:23], v[160:161], v[18:19]
	v_pk_mul_f32 v[8:9], v[26:27], s[16:17] op_sel_hi:[1,0]
	v_med3_f32 v22, v22, s63, v195
	v_med3_f32 v23, v23, s63, v195
	v_cvt_pk_fp8_f32 v30, v22, v23 op_sel:[0,0,1]
	v_pk_mul_f32 v[22:23], v[126:127], v[8:9]
	v_pk_mul_f32 v[6:7], v[28:29], s[16:17] op_sel_hi:[1,0]
	v_pk_mul_f32 v[28:29], v[154:155], v[16:17]
	v_pk_mul_f32 v[144:145], v[144:145], v[10:11]
	v_pk_mul_f32 v[142:143], v[142:143], v[12:13]
	v_pk_mul_f32 v[150:151], v[150:151], v[20:21]
	v_pk_mul_f32 v[146:147], v[146:147], v[16:17]
	v_pk_mul_f32 v[134:135], v[134:135], v[12:13]
	v_med3_f32 v5, v22, s63, v195
	v_med3_f32 v22, v23, s63, v195
	v_med3_f32 v25, v28, s63, v195
	v_med3_f32 v28, v29, s63, v195
	v_med3_f32 v29, v142, s63, v195
	v_med3_f32 v142, v143, s63, v195
	v_med3_f32 v143, v144, s63, v195
	v_med3_f32 v144, v145, s63, v195
	v_med3_f32 v145, v150, s63, v195
	v_med3_f32 v150, v151, s63, v195
	v_med3_f32 v146, v146, s63, v195
	v_med3_f32 v147, v147, s63, v195
	v_med3_f32 v134, v134, s63, v195
	v_med3_f32 v135, v135, s63, v195
	v_cvt_pk_fp8_f32 v199, v5, v22
	v_cvt_pk_fp8_f32 v196, v145, v150
	v_cvt_pk_fp8_f32 v197, v146, v147
	v_cvt_pk_fp8_f32 v198, v134, v135
	v_pk_mul_f32 v[22:23], v[128:129], v[6:7]
	v_pk_mul_f32 v[152:153], v[152:153], v[18:19]
	v_pk_mul_f32 v[148:149], v[148:149], v[14:15]
	v_pk_mul_f32 v[136:137], v[136:137], v[10:11]
	v_med3_f32 v5, v22, s63, v195
	v_med3_f32 v22, v23, s63, v195
	v_med3_f32 v151, v152, s63, v195
	v_med3_f32 v152, v153, s63, v195
	v_med3_f32 v148, v148, s63, v195
	v_med3_f32 v149, v149, s63, v195
	v_med3_f32 v136, v136, s63, v195
	v_med3_f32 v137, v137, s63, v195
	v_cvt_pk_fp8_f32 v199, v5, v22 op_sel:[0,0,1]
	v_or_b32_e32 v22, 16, v4
	v_cvt_pk_fp8_f32 v196, v151, v152 op_sel:[0,0,1]
	v_cvt_pk_fp8_f32 v197, v148, v149 op_sel:[0,0,1]
	v_cvt_pk_fp8_f32 v198, v136, v137 op_sel:[0,0,1]
	v_ashrrev_i32_e32 v23, 31, v22
	v_lshlrev_b64 v[22:23], 11, v[22:23]
	v_lshl_add_u64 v[22:23], s[10:11], 0, v[22:23]
	v_lshl_add_u64 v[22:23], v[22:23], 0, v[2:3]
	global_store_dwordx4 v[22:23], v[196:199], off
	v_pk_mul_f32 v[22:23], v[130:131], v[20:21]
	v_cvt_pk_fp8_f32 v31, v25, v28
	v_med3_f32 v5, v22, s63, v195
	v_med3_f32 v23, v23, s63, v195
	v_mov_b32_e32 v22, 0
	v_cvt_pk_fp8_f32 v22, v5, v23
	v_pk_mul_f32 v[24:25], v[132:133], v[18:19]
	v_pk_mul_f32 v[26:27], v[156:157], v[14:15]
	v_med3_f32 v5, v24, s63, v195
	v_med3_f32 v23, v25, s63, v195
	v_pk_mul_f32 v[24:25], v[122:123], v[16:17]
	v_cvt_pk_fp8_f32 v22, v5, v23 op_sel:[0,0,1]
	v_med3_f32 v5, v24, s63, v195
	v_med3_f32 v24, v25, s63, v195
	v_mov_b32_e32 v23, 0
	v_cvt_pk_fp8_f32 v23, v5, v24
	v_pk_mul_f32 v[24:25], v[124:125], v[14:15]
	v_med3_f32 v26, v26, s63, v195
	v_med3_f32 v5, v24, s63, v195
	v_med3_f32 v24, v25, s63, v195
	v_cvt_pk_fp8_f32 v23, v5, v24 op_sel:[0,0,1]
	v_pk_mul_f32 v[24:25], v[118:119], v[12:13]
	v_med3_f32 v27, v27, s63, v195
	v_med3_f32 v5, v24, s63, v195
	v_med3_f32 v25, v25, s63, v195
	v_mov_b32_e32 v24, 0
	v_cvt_pk_fp8_f32 v24, v5, v25
	v_cvt_pk_fp8_f32 v31, v26, v27 op_sel:[0,0,1]
	v_pk_mul_f32 v[26:27], v[120:121], v[10:11]
	v_cvt_pk_fp8_f32 v32, v29, v142
	v_med3_f32 v5, v26, s63, v195
	v_med3_f32 v25, v27, s63, v195
	v_pk_mul_f32 v[26:27], v[110:111], v[8:9]
	v_cvt_pk_fp8_f32 v24, v5, v25 op_sel:[0,0,1]
	v_med3_f32 v5, v26, s63, v195
	v_med3_f32 v26, v27, s63, v195
	v_mov_b32_e32 v25, 0
	v_cvt_pk_fp8_f32 v25, v5, v26
	v_pk_mul_f32 v[26:27], v[112:113], v[6:7]
	v_pk_mul_f32 v[28:29], v[88:89], v[10:11]
	v_med3_f32 v5, v26, s63, v195
	v_med3_f32 v26, v27, s63, v195
	v_cvt_pk_fp8_f32 v25, v5, v26 op_sel:[0,0,1]
	v_or_b32_e32 v26, 32, v4
	v_ashrrev_i32_e32 v27, 31, v26
	v_lshlrev_b64 v[26:27], 11, v[26:27]
	v_lshl_add_u64 v[26:27], s[10:11], 0, v[26:27]
	v_lshl_add_u64 v[26:27], v[26:27], 0, v[2:3]
	global_store_dwordx4 v[26:27], v[22:25], off
	v_pk_mul_f32 v[26:27], v[104:105], v[10:11]
	v_pk_mul_f32 v[138:139], v[138:139], v[8:9]
	v_pk_mul_f32 v[22:23], v[114:115], v[20:21]
	v_pk_mul_f32 v[24:25], v[116:117], v[18:19]
	v_med3_f32 v5, v22, s63, v195
; __device__ __forceinline__ unsigned pk4_fp8(float a, float b, float c, float d) { int w = 0; w = __builtin_amdgcn_cvt_pk_fp8_f32(clamp8(a), clamp8(b), w, false); w = __builtin_amdgcn_cvt_pk_fp8_f32(clamp8(c), clamp8(d), w, true); return (unsigned)w; }
; __device__ __forceinline__ float clamp8(float x) { return __builtin_amdgcn_fmed3f(x, -448.0f, 448.0f); }
;     __device__ __forceinline__ void operator()(AccRef acc, const GUnit& u, int wr, int wc, int fr, int fq) const {
;     ...
;         for (int ai = 0; ai < 2; ++ai)
; #pragma unroll
;             for (int m = 0; m < 4; ++m) { u32x4 w;
; #pragma unroll
;                 for (int q = 0; q < 4; ++q) { const f32x4 v = acc[ai][q >> 1][m][q & 1] * gv[q]; w[q] = pk4_fp8(v[0], v[1], v[2], v[3]); }
;                 *(u32x4*)(MG + (size_t)(pm * 256 + ai * 128 + wr * 64 + m * 16 + fr) * D + col0) = w; }
	v_med3_f32 v23, v23, s63, v195
	v_mov_b32_e32 v22, 0
	v_cvt_pk_fp8_f32 v22, v5, v23
	v_med3_f32 v5, v24, s63, v195
	v_med3_f32 v23, v25, s63, v195
	v_pk_mul_f32 v[24:25], v[106:107], v[16:17]
	v_cvt_pk_fp8_f32 v22, v5, v23 op_sel:[0,0,1]
	v_med3_f32 v5, v24, s63, v195
	v_med3_f32 v24, v25, s63, v195
	v_mov_b32_e32 v23, 0
	v_cvt_pk_fp8_f32 v23, v5, v24
	v_pk_mul_f32 v[24:25], v[108:109], v[14:15]
	v_med3_f32 v138, v138, s63, v195
	v_med3_f32 v5, v24, s63, v195
	v_med3_f32 v24, v25, s63, v195
	v_cvt_pk_fp8_f32 v23, v5, v24 op_sel:[0,0,1]
	v_pk_mul_f32 v[24:25], v[102:103], v[12:13]
	v_med3_f32 v139, v139, s63, v195
	v_med3_f32 v5, v24, s63, v195
	v_med3_f32 v25, v25, s63, v195
	v_mov_b32_e32 v24, 0
	v_cvt_pk_fp8_f32 v24, v5, v25
	v_med3_f32 v5, v26, s63, v195
	v_med3_f32 v25, v27, s63, v195
	v_pk_mul_f32 v[26:27], v[98:99], v[8:9]
	v_cvt_pk_fp8_f32 v24, v5, v25 op_sel:[0,0,1]
	v_med3_f32 v5, v26, s63, v195
	v_med3_f32 v26, v27, s63, v195
	v_mov_b32_e32 v25, 0
	v_cvt_pk_fp8_f32 v25, v5, v26
	v_pk_mul_f32 v[26:27], v[100:101], v[6:7]
	v_cvt_pk_fp8_f32 v33, v138, v139
	v_med3_f32 v5, v26, s63, v195
	v_med3_f32 v26, v27, s63, v195
	v_cvt_pk_fp8_f32 v25, v5, v26 op_sel:[0,0,1]
	v_or_b32_e32 v26, 48, v4
	v_ashrrev_i32_e32 v27, 31, v26
	v_lshlrev_b64 v[26:27], 11, v[26:27]
	v_lshl_add_u64 v[26:27], s[10:11], 0, v[26:27]
	v_lshl_add_u64 v[26:27], v[26:27], 0, v[2:3]
	global_store_dwordx4 v[26:27], v[22:25], off
	v_add_u32_e32 v26, 0x80, v4
	v_pk_mul_f32 v[140:141], v[140:141], v[6:7]
	v_pk_mul_f32 v[22:23], v[94:95], v[20:21]
	v_pk_mul_f32 v[24:25], v[96:97], v[18:19]
	v_med3_f32 v5, v22, s63, v195
	v_med3_f32 v23, v23, s63, v195
	v_mov_b32_e32 v22, 0
	v_cvt_pk_fp8_f32 v22, v5, v23
	v_med3_f32 v5, v24, s63, v195
	v_med3_f32 v23, v25, s63, v195
	v_pk_mul_f32 v[24:25], v[90:91], v[16:17]
	v_cvt_pk_fp8_f32 v22, v5, v23 op_sel:[0,0,1]
	v_med3_f32 v5, v24, s63, v195
	v_med3_f32 v24, v25, s63, v195
	v_mov_b32_e32 v23, 0
	v_cvt_pk_fp8_f32 v23, v5, v24
	v_pk_mul_f32 v[24:25], v[92:93], v[14:15]
	v_med3_f32 v140, v140, s63, v195
	v_med3_f32 v5, v24, s63, v195
	v_med3_f32 v24, v25, s63, v195
	v_cvt_pk_fp8_f32 v23, v5, v24 op_sel:[0,0,1]
	v_pk_mul_f32 v[24:25], v[86:87], v[12:13]
	v_med3_f32 v141, v141, s63, v195
	v_med3_f32 v5, v24, s63, v195
	v_med3_f32 v25, v25, s63, v195
	v_mov_b32_e32 v24, 0
	v_cvt_pk_fp8_f32 v24, v5, v25
	v_med3_f32 v5, v28, s63, v195
	v_med3_f32 v25, v29, s63, v195
	v_pk_mul_f32 v[28:29], v[78:79], v[8:9]
	v_cvt_pk_fp8_f32 v24, v5, v25 op_sel:[0,0,1]
	v_med3_f32 v5, v28, s63, v195
	v_med3_f32 v27, v29, s63, v195
	v_mov_b32_e32 v25, 0
	v_cvt_pk_fp8_f32 v25, v5, v27
	v_pk_mul_f32 v[28:29], v[80:81], v[6:7]
	v_cvt_pk_fp8_f32 v32, v143, v144 op_sel:[0,0,1]
	v_med3_f32 v5, v28, s63, v195
	v_med3_f32 v27, v29, s63, v195
	v_cvt_pk_fp8_f32 v25, v5, v27 op_sel:[0,0,1]
	v_ashrrev_i32_e32 v27, 31, v26
	v_lshlrev_b64 v[26:27], 11, v[26:27]
	v_lshl_add_u64 v[26:27], s[10:11], 0, v[26:27]
	v_lshl_add_u64 v[26:27], v[26:27], 0, v[2:3]
	global_store_dwordx4 v[26:27], v[22:25], off
	v_pk_mul_f32 v[26:27], v[72:73], v[10:11]
	v_cvt_pk_fp8_f32 v33, v140, v141 op_sel:[0,0,1]
	v_pk_mul_f32 v[22:23], v[82:83], v[20:21]
	v_pk_mul_f32 v[24:25], v[84:85], v[18:19]
	v_med3_f32 v5, v22, s63, v195
	v_med3_f32 v23, v23, s63, v195
	v_mov_b32_e32 v22, 0
	v_cvt_pk_fp8_f32 v22, v5, v23
	v_med3_f32 v5, v24, s63, v195
	v_med3_f32 v23, v25, s63, v195
	v_pk_mul_f32 v[24:25], v[74:75], v[16:17]
	v_cvt_pk_fp8_f32 v22, v5, v23 op_sel:[0,0,1]
	v_med3_f32 v5, v24, s63, v195
	v_med3_f32 v24, v25, s63, v195
	v_mov_b32_e32 v23, 0
	v_cvt_pk_fp8_f32 v23, v5, v24
	v_pk_mul_f32 v[24:25], v[76:77], v[14:15]
	global_store_dwordx4 v[200:201], v[30:33], off
	v_med3_f32 v5, v24, s63, v195
	v_med3_f32 v24, v25, s63, v195
	v_cvt_pk_fp8_f32 v23, v5, v24 op_sel:[0,0,1]
	v_pk_mul_f32 v[24:25], v[70:71], v[12:13]
	s_nop 0
	v_med3_f32 v5, v24, s63, v195
	v_med3_f32 v25, v25, s63, v195
	v_mov_b32_e32 v24, 0
	v_cvt_pk_fp8_f32 v24, v5, v25
	v_med3_f32 v5, v26, s63, v195
	v_med3_f32 v25, v27, s63, v195
	v_pk_mul_f32 v[26:27], v[62:63], v[8:9]
	v_cvt_pk_fp8_f32 v24, v5, v25 op_sel:[0,0,1]
	v_med3_f32 v5, v26, s63, v195
	v_med3_f32 v26, v27, s63, v195
	v_mov_b32_e32 v25, 0
	v_cvt_pk_fp8_f32 v25, v5, v26
	v_pk_mul_f32 v[26:27], v[64:65], v[6:7]
	s_nop 0
	v_med3_f32 v5, v26, s63, v195
	v_med3_f32 v26, v27, s63, v195
	v_cvt_pk_fp8_f32 v25, v5, v26 op_sel:[0,0,1]
	v_add_u32_e32 v26, 0x90, v4
	v_ashrrev_i32_e32 v27, 31, v26
	v_lshlrev_b64 v[26:27], 11, v[26:27]
	v_lshl_add_u64 v[26:27], s[10:11], 0, v[26:27]
	v_lshl_add_u64 v[26:27], v[26:27], 0, v[2:3]
	global_store_dwordx4 v[26:27], v[22:25], off
	v_pk_mul_f32 v[26:27], v[56:57], v[10:11]
	v_pk_mul_f32 v[10:11], v[40:41], v[10:11]
	v_pk_mul_f32 v[22:23], v[66:67], v[20:21]
	v_pk_mul_f32 v[24:25], v[68:69], v[18:19]
	v_med3_f32 v5, v22, s63, v195
	v_med3_f32 v23, v23, s63, v195
	v_mov_b32_e32 v22, 0
	v_cvt_pk_fp8_f32 v22, v5, v23
	v_med3_f32 v5, v24, s63, v195
	v_med3_f32 v23, v25, s63, v195
	v_pk_mul_f32 v[24:25], v[58:59], v[16:17]
	v_cvt_pk_fp8_f32 v22, v5, v23 op_sel:[0,0,1]
	v_med3_f32 v5, v24, s63, v195
	v_med3_f32 v24, v25, s63, v195
	v_mov_b32_e32 v23, 0
	v_cvt_pk_fp8_f32 v23, v5, v24
	v_pk_mul_f32 v[24:25], v[60:61], v[14:15]
	v_pk_mul_f32 v[20:21], v[50:51], v[20:21]
	v_med3_f32 v5, v24, s63, v195
	v_med3_f32 v24, v25, s63, v195
	v_cvt_pk_fp8_f32 v23, v5, v24 op_sel:[0,0,1]
	v_pk_mul_f32 v[24:25], v[54:55], v[12:13]
	v_med3_f32 v21, v21, s63, v195
	v_med3_f32 v5, v24, s63, v195
	v_med3_f32 v25, v25, s63, v195
	v_mov_b32_e32 v24, 0
	v_cvt_pk_fp8_f32 v24, v5, v25
	v_med3_f32 v5, v26, s63, v195
	v_med3_f32 v25, v27, s63, v195
; __device__ __forceinline__ unsigned pk4_fp8(float a, float b, float c, float d) { int w = 0; w = __builtin_amdgcn_cvt_pk_fp8_f32(clamp8(a), clamp8(b), w, false); w = __builtin_amdgcn_cvt_pk_fp8_f32(clamp8(c), clamp8(d), w, true); return (unsigned)w; }
; __device__ __forceinline__ float clamp8(float x) { return __builtin_amdgcn_fmed3f(x, -448.0f, 448.0f); }
;     __device__ __forceinline__ void operator()(AccRef acc, const GUnit& u, int wr, int wc, int fr, int fq) const {
;     ...
;         for (int ai = 0; ai < 2; ++ai)
; #pragma unroll
;             for (int m = 0; m < 4; ++m) { u32x4 w;
; #pragma unroll
;                 for (int q = 0; q < 4; ++q) { const f32x4 v = acc[ai][q >> 1][m][q & 1] * gv[q]; w[q] = pk4_fp8(v[0], v[1], v[2], v[3]); }
;                 *(u32x4*)(MG + (size_t)(pm * 256 + ai * 128 + wr * 64 + m * 16 + fr) * D + col0) = w; }
	v_pk_mul_f32 v[26:27], v[46:47], v[8:9]
	v_cvt_pk_fp8_f32 v24, v5, v25 op_sel:[0,0,1]
	v_med3_f32 v5, v26, s63, v195
	v_med3_f32 v26, v27, s63, v195
	v_mov_b32_e32 v25, 0
	v_cvt_pk_fp8_f32 v25, v5, v26
	v_pk_mul_f32 v[26:27], v[48:49], v[6:7]
	v_pk_mul_f32 v[18:19], v[52:53], v[18:19]
	v_med3_f32 v5, v26, s63, v195
	v_med3_f32 v26, v27, s63, v195
	v_cvt_pk_fp8_f32 v25, v5, v26 op_sel:[0,0,1]
	v_med3_f32 v5, v20, s63, v195
	v_mov_b32_e32 v20, 0
	v_cvt_pk_fp8_f32 v20, v5, v21
	v_med3_f32 v5, v18, s63, v195
	v_med3_f32 v18, v19, s63, v195
	v_pk_mul_f32 v[16:17], v[42:43], v[16:17]
	v_add_u32_e32 v26, 0xa0, v4
	v_cvt_pk_fp8_f32 v20, v5, v18 op_sel:[0,0,1]
	v_med3_f32 v5, v16, s63, v195
	v_med3_f32 v16, v17, s63, v195
	v_mov_b32_e32 v21, 0
	v_ashrrev_i32_e32 v27, 31, v26
	v_cvt_pk_fp8_f32 v21, v5, v16
	v_lshlrev_b64 v[26:27], 11, v[26:27]
	v_lshl_add_u64 v[26:27], s[10:11], 0, v[26:27]
	v_pk_mul_f32 v[14:15], v[44:45], v[14:15]
	v_lshl_add_u64 v[26:27], v[26:27], 0, v[2:3]
	v_med3_f32 v5, v14, s63, v195
	v_med3_f32 v14, v15, s63, v195
	v_pk_mul_f32 v[12:13], v[38:39], v[12:13]
	global_store_dwordx4 v[26:27], v[22:25], off
	v_cvt_pk_fp8_f32 v21, v5, v14 op_sel:[0,0,1]
	v_med3_f32 v5, v12, s63, v195
	v_med3_f32 v12, v13, s63, v195
	v_mov_b32_e32 v22, 0
	v_cvt_pk_fp8_f32 v22, v5, v12
	v_med3_f32 v5, v10, s63, v195
	v_med3_f32 v10, v11, s63, v195
	v_pk_mul_f32 v[8:9], v[34:35], v[8:9]
	v_cvt_pk_fp8_f32 v22, v5, v10 op_sel:[0,0,1]
	v_med3_f32 v5, v8, s63, v195
	v_med3_f32 v8, v9, s63, v195
	v_mov_b32_e32 v23, 0
	v_cvt_pk_fp8_f32 v23, v5, v8
	v_pk_mul_f32 v[6:7], v[36:37], v[6:7]
	v_add_u32_e32 v4, 0xb0, v4
	v_med3_f32 v5, v6, s63, v195
	v_med3_f32 v6, v7, s63, v195
	v_cvt_pk_fp8_f32 v23, v5, v6 op_sel:[0,0,1]
	v_ashrrev_i32_e32 v5, 31, v4
	v_lshlrev_b64 v[4:5], 11, v[4:5]
	v_lshl_add_u64 v[4:5], s[10:11], 0, v[4:5]
	v_lshl_add_u64 v[2:3], v[4:5], 0, v[2:3]
	global_store_dwordx4 v[2:3], v[20:23], off
.Lwtj_o:
	s_cbranch_vccnz .LBB0_903
	s_andn2_b64 vcc, exec, s[8:9]
	s_cbranch_vccnz .LBB0_902
	s_branch .LBB0_902
.Lwt_o:
	s_ashr_i32 s19, s26, 5
	s_mul_hi_i32 s21, s19, 0xc000
	s_mul_i32 s19, s19, 0xc000
	s_add_u32 s28, s36, s19
	v_lshl_or_b32 v2, s64, 8, v190
	s_addc_u32 s29, s37, s21
	v_ashrrev_i32_e32 v3, 31, v2
	v_lshl_add_u64 v[4:5], v[2:3], 2, s[28:29]
	v_add_co_u32_e32 v6, vcc, s62, v4
	s_nop 15
	s_nop 7
	s_nop 1
	v_addc_co_u32_e32 v7, vcc, 0, v5, vcc
	global_load_dwordx4 v[6:9], v[6:7], off
	v_lshl_add_u64 v[4:5], v[4:5], 0, s[14:15]
	global_load_dwordx4 v[10:13], v[4:5], off offset:16
	global_load_dwordx4 v[22:25], v[4:5], off offset:32
	global_load_dwordx4 v[26:29], v[4:5], off offset:48
	v_lshl_add_u32 v4, s26, 8, v188
	v_ashrrev_i32_e32 v5, 31, v4
	v_mov_b32_e32 v30, 0
	v_lshlrev_b64 v[14:15], 11, v[4:5]
	v_lshl_add_u64 v[14:15], s[10:11], 0, v[14:15]
	v_lshl_add_u64 v[200:201], v[14:15], 0, v[2:3]
	v_mov_b32_e32 v199, 0
	v_mov_b32_e32 v196, 0
	v_mov_b32_e32 v197, 0
	v_mov_b32_e32 v198, 0
	v_mov_b32_e32 v31, 0
	v_mov_b32_e32 v32, 0
	v_mov_b32_e32 v33, 0
	s_andn2_b64 vcc, exec, s[0:1]
	s_mov_b64 s[0:1], -1
	s_waitcnt vmcnt(0) lgkmcnt(0)
	v_pk_mul_f32 v[16:17], v[10:11], s[16:17] op_sel_hi:[1,0]
	v_pk_mul_f32 v[20:21], v[6:7], s[16:17] op_sel_hi:[1,0]
	v_pk_mul_f32 v[10:11], v[24:25], s[16:17] op_sel_hi:[1,0]
	v_pk_mul_f32 v[24:25], v[158:159], v[20:21]
	v_pk_mul_f32 v[18:19], v[8:9], s[16:17] op_sel_hi:[1,0]
	v_med3_f32 v5, v24, s63, v195
	v_med3_f32 v24, v25, s63, v195
	v_cvt_pk_fp8_f32 v30, v5, v24
	v_pk_mul_f32 v[14:15], v[12:13], s[16:17] op_sel_hi:[1,0]
	v_pk_mul_f32 v[12:13], v[22:23], s[16:17] op_sel_hi:[1,0]
	v_pk_mul_f32 v[22:23], v[160:161], v[18:19]
	v_pk_mul_f32 v[8:9], v[26:27], s[16:17] op_sel_hi:[1,0]
	v_med3_f32 v22, v22, s63, v195
	v_med3_f32 v23, v23, s63, v195
	v_cvt_pk_fp8_f32 v30, v22, v23 op_sel:[0,0,1]
	v_pk_mul_f32 v[22:23], v[126:127], v[8:9]
	v_pk_mul_f32 v[6:7], v[28:29], s[16:17] op_sel_hi:[1,0]
	v_pk_mul_f32 v[28:29], v[154:155], v[16:17]
	v_pk_mul_f32 v[144:145], v[144:145], v[10:11]
	v_pk_mul_f32 v[142:143], v[142:143], v[12:13]
	v_pk_mul_f32 v[150:151], v[150:151], v[20:21]
	v_pk_mul_f32 v[146:147], v[146:147], v[16:17]
	v_pk_mul_f32 v[134:135], v[134:135], v[12:13]
	v_med3_f32 v5, v22, s63, v195
	v_med3_f32 v22, v23, s63, v195
	v_med3_f32 v25, v28, s63, v195
	v_med3_f32 v28, v29, s63, v195
	v_med3_f32 v29, v142, s63, v195
	v_med3_f32 v142, v143, s63, v195
	v_med3_f32 v143, v144, s63, v195
	v_med3_f32 v144, v145, s63, v195
	v_med3_f32 v145, v150, s63, v195
	v_med3_f32 v150, v151, s63, v195
	v_med3_f32 v146, v146, s63, v195
	v_med3_f32 v147, v147, s63, v195
	v_med3_f32 v134, v134, s63, v195
	v_med3_f32 v135, v135, s63, v195
	v_cvt_pk_fp8_f32 v199, v5, v22
	v_cvt_pk_fp8_f32 v196, v145, v150
	v_cvt_pk_fp8_f32 v197, v146, v147
	v_cvt_pk_fp8_f32 v198, v134, v135
	v_pk_mul_f32 v[22:23], v[128:129], v[6:7]
	v_pk_mul_f32 v[152:153], v[152:153], v[18:19]
	v_pk_mul_f32 v[148:149], v[148:149], v[14:15]
	v_pk_mul_f32 v[136:137], v[136:137], v[10:11]
	v_med3_f32 v5, v22, s63, v195
	v_med3_f32 v22, v23, s63, v195
	v_med3_f32 v151, v152, s63, v195
	v_med3_f32 v152, v153, s63, v195
	v_med3_f32 v148, v148, s63, v195
	v_med3_f32 v149, v149, s63, v195
	v_med3_f32 v136, v136, s63, v195
	v_med3_f32 v137, v137, s63, v195
	v_cvt_pk_fp8_f32 v199, v5, v22 op_sel:[0,0,1]
	v_or_b32_e32 v22, 16, v4
	v_cvt_pk_fp8_f32 v196, v151, v152 op_sel:[0,0,1]
	v_cvt_pk_fp8_f32 v197, v148, v149 op_sel:[0,0,1]
	v_cvt_pk_fp8_f32 v198, v136, v137 op_sel:[0,0,1]
	v_ashrrev_i32_e32 v23, 31, v22
	v_lshlrev_b64 v[22:23], 11, v[22:23]
	v_lshl_add_u64 v[22:23], s[10:11], 0, v[22:23]
	v_lshl_add_u64 v[22:23], v[22:23], 0, v[2:3]
; __device__ __forceinline__ unsigned pk4_fp8(float a, float b, float c, float d) { int w = 0; w = __builtin_amdgcn_cvt_pk_fp8_f32(clamp8(a), clamp8(b), w, false); w = __builtin_amdgcn_cvt_pk_fp8_f32(clamp8(c), clamp8(d), w, true); return (unsigned)w; }
; __device__ __forceinline__ float clamp8(float x) { return __builtin_amdgcn_fmed3f(x, -448.0f, 448.0f); }
;     __device__ __forceinline__ void operator()(AccRef acc, const GUnit& u, int wr, int wc, int fr, int fq) const {
;     ...
;         for (int ai = 0; ai < 2; ++ai)
; #pragma unroll
;             for (int m = 0; m < 4; ++m) { u32x4 w;
; #pragma unroll
;                 for (int q = 0; q < 4; ++q) { const f32x4 v = acc[ai][q >> 1][m][q & 1] * gv[q]; w[q] = pk4_fp8(v[0], v[1], v[2], v[3]); }
;                 *(u32x4*)(MG + (size_t)(pm * 256 + ai * 128 + wr * 64 + m * 16 + fr) * D + col0) = w; }
	global_store_dwordx4 v[22:23], v[196:199], off sc1
	v_pk_mul_f32 v[22:23], v[130:131], v[20:21]
	v_cvt_pk_fp8_f32 v31, v25, v28
	v_med3_f32 v5, v22, s63, v195
	v_med3_f32 v23, v23, s63, v195
	v_mov_b32_e32 v22, 0
	v_cvt_pk_fp8_f32 v22, v5, v23
	v_pk_mul_f32 v[24:25], v[132:133], v[18:19]
	v_pk_mul_f32 v[26:27], v[156:157], v[14:15]
	v_med3_f32 v5, v24, s63, v195
	v_med3_f32 v23, v25, s63, v195
	v_pk_mul_f32 v[24:25], v[122:123], v[16:17]
	v_cvt_pk_fp8_f32 v22, v5, v23 op_sel:[0,0,1]
	v_med3_f32 v5, v24, s63, v195
	v_med3_f32 v24, v25, s63, v195
	v_mov_b32_e32 v23, 0
	v_cvt_pk_fp8_f32 v23, v5, v24
	v_pk_mul_f32 v[24:25], v[124:125], v[14:15]
	v_med3_f32 v26, v26, s63, v195
	v_med3_f32 v5, v24, s63, v195
	v_med3_f32 v24, v25, s63, v195
	v_cvt_pk_fp8_f32 v23, v5, v24 op_sel:[0,0,1]
	v_pk_mul_f32 v[24:25], v[118:119], v[12:13]
	v_med3_f32 v27, v27, s63, v195
	v_med3_f32 v5, v24, s63, v195
	v_med3_f32 v25, v25, s63, v195
	v_mov_b32_e32 v24, 0
	v_cvt_pk_fp8_f32 v24, v5, v25
	v_cvt_pk_fp8_f32 v31, v26, v27 op_sel:[0,0,1]
	v_pk_mul_f32 v[26:27], v[120:121], v[10:11]
	v_cvt_pk_fp8_f32 v32, v29, v142
	v_med3_f32 v5, v26, s63, v195
	v_med3_f32 v25, v27, s63, v195
	v_pk_mul_f32 v[26:27], v[110:111], v[8:9]
	v_cvt_pk_fp8_f32 v24, v5, v25 op_sel:[0,0,1]
	v_med3_f32 v5, v26, s63, v195
	v_med3_f32 v26, v27, s63, v195
	v_mov_b32_e32 v25, 0
	v_cvt_pk_fp8_f32 v25, v5, v26
	v_pk_mul_f32 v[26:27], v[112:113], v[6:7]
	v_pk_mul_f32 v[28:29], v[88:89], v[10:11]
	v_med3_f32 v5, v26, s63, v195
	v_med3_f32 v26, v27, s63, v195
	v_cvt_pk_fp8_f32 v25, v5, v26 op_sel:[0,0,1]
	v_or_b32_e32 v26, 32, v4
	v_ashrrev_i32_e32 v27, 31, v26
	v_lshlrev_b64 v[26:27], 11, v[26:27]
	v_lshl_add_u64 v[26:27], s[10:11], 0, v[26:27]
	v_lshl_add_u64 v[26:27], v[26:27], 0, v[2:3]
	global_store_dwordx4 v[26:27], v[22:25], off sc1
	v_pk_mul_f32 v[26:27], v[104:105], v[10:11]
	v_pk_mul_f32 v[138:139], v[138:139], v[8:9]
	v_pk_mul_f32 v[22:23], v[114:115], v[20:21]
	v_pk_mul_f32 v[24:25], v[116:117], v[18:19]
	v_med3_f32 v5, v22, s63, v195
	v_med3_f32 v23, v23, s63, v195
	v_mov_b32_e32 v22, 0
	v_cvt_pk_fp8_f32 v22, v5, v23
	v_med3_f32 v5, v24, s63, v195
	v_med3_f32 v23, v25, s63, v195
	v_pk_mul_f32 v[24:25], v[106:107], v[16:17]
	v_cvt_pk_fp8_f32 v22, v5, v23 op_sel:[0,0,1]
	v_med3_f32 v5, v24, s63, v195
	v_med3_f32 v24, v25, s63, v195
	v_mov_b32_e32 v23, 0
	v_cvt_pk_fp8_f32 v23, v5, v24
	v_pk_mul_f32 v[24:25], v[108:109], v[14:15]
	v_med3_f32 v138, v138, s63, v195
	v_med3_f32 v5, v24, s63, v195
	v_med3_f32 v24, v25, s63, v195
	v_cvt_pk_fp8_f32 v23, v5, v24 op_sel:[0,0,1]
	v_pk_mul_f32 v[24:25], v[102:103], v[12:13]
	v_med3_f32 v139, v139, s63, v195
	v_med3_f32 v5, v24, s63, v195
	v_med3_f32 v25, v25, s63, v195
	v_mov_b32_e32 v24, 0
	v_cvt_pk_fp8_f32 v24, v5, v25
	v_med3_f32 v5, v26, s63, v195
	v_med3_f32 v25, v27, s63, v195
	v_pk_mul_f32 v[26:27], v[98:99], v[8:9]
	v_cvt_pk_fp8_f32 v24, v5, v25 op_sel:[0,0,1]
	v_med3_f32 v5, v26, s63, v195
	v_med3_f32 v26, v27, s63, v195
	v_mov_b32_e32 v25, 0
	v_cvt_pk_fp8_f32 v25, v5, v26
	v_pk_mul_f32 v[26:27], v[100:101], v[6:7]
	v_cvt_pk_fp8_f32 v33, v138, v139
	v_med3_f32 v5, v26, s63, v195
	v_med3_f32 v26, v27, s63, v195
	v_cvt_pk_fp8_f32 v25, v5, v26 op_sel:[0,0,1]
	v_or_b32_e32 v26, 48, v4
	v_ashrrev_i32_e32 v27, 31, v26
	v_lshlrev_b64 v[26:27], 11, v[26:27]
	v_lshl_add_u64 v[26:27], s[10:11], 0, v[26:27]
	v_lshl_add_u64 v[26:27], v[26:27], 0, v[2:3]
	global_store_dwordx4 v[26:27], v[22:25], off sc1
	v_add_u32_e32 v26, 0x80, v4
	v_pk_mul_f32 v[140:141], v[140:141], v[6:7]
	v_pk_mul_f32 v[22:23], v[94:95], v[20:21]
	v_pk_mul_f32 v[24:25], v[96:97], v[18:19]
	v_med3_f32 v5, v22, s63, v195
	v_med3_f32 v23, v23, s63, v195
	v_mov_b32_e32 v22, 0
	v_cvt_pk_fp8_f32 v22, v5, v23
	v_med3_f32 v5, v24, s63, v195
	v_med3_f32 v23, v25, s63, v195
	v_pk_mul_f32 v[24:25], v[90:91], v[16:17]
	v_cvt_pk_fp8_f32 v22, v5, v23 op_sel:[0,0,1]
	v_med3_f32 v5, v24, s63, v195
	v_med3_f32 v24, v25, s63, v195
	v_mov_b32_e32 v23, 0
	v_cvt_pk_fp8_f32 v23, v5, v24
	v_pk_mul_f32 v[24:25], v[92:93], v[14:15]
	v_med3_f32 v140, v140, s63, v195
	v_med3_f32 v5, v24, s63, v195
	v_med3_f32 v24, v25, s63, v195
	v_cvt_pk_fp8_f32 v23, v5, v24 op_sel:[0,0,1]
	v_pk_mul_f32 v[24:25], v[86:87], v[12:13]
	v_med3_f32 v141, v141, s63, v195
	v_med3_f32 v5, v24, s63, v195
	v_med3_f32 v25, v25, s63, v195
	v_mov_b32_e32 v24, 0
	v_cvt_pk_fp8_f32 v24, v5, v25
	v_med3_f32 v5, v28, s63, v195
	v_med3_f32 v25, v29, s63, v195
	v_pk_mul_f32 v[28:29], v[78:79], v[8:9]
	v_cvt_pk_fp8_f32 v24, v5, v25 op_sel:[0,0,1]
	v_med3_f32 v5, v28, s63, v195
	v_med3_f32 v27, v29, s63, v195
	v_mov_b32_e32 v25, 0
	v_cvt_pk_fp8_f32 v25, v5, v27
	v_pk_mul_f32 v[28:29], v[80:81], v[6:7]
	v_cvt_pk_fp8_f32 v32, v143, v144 op_sel:[0,0,1]
	v_med3_f32 v5, v28, s63, v195
	v_med3_f32 v27, v29, s63, v195
; __device__ __forceinline__ unsigned pk4_fp8(float a, float b, float c, float d) { int w = 0; w = __builtin_amdgcn_cvt_pk_fp8_f32(clamp8(a), clamp8(b), w, false); w = __builtin_amdgcn_cvt_pk_fp8_f32(clamp8(c), clamp8(d), w, true); return (unsigned)w; }
; __device__ __forceinline__ float clamp8(float x) { return __builtin_amdgcn_fmed3f(x, -448.0f, 448.0f); }
;     __device__ __forceinline__ void operator()(AccRef acc, const GUnit& u, int wr, int wc, int fr, int fq) const {
;     ...
;         for (int ai = 0; ai < 2; ++ai)
; #pragma unroll
;             for (int m = 0; m < 4; ++m) { u32x4 w;
; #pragma unroll
;                 for (int q = 0; q < 4; ++q) { const f32x4 v = acc[ai][q >> 1][m][q & 1] * gv[q]; w[q] = pk4_fp8(v[0], v[1], v[2], v[3]); }
;                 *(u32x4*)(MG + (size_t)(pm * 256 + ai * 128 + wr * 64 + m * 16 + fr) * D + col0) = w; }
	v_cvt_pk_fp8_f32 v25, v5, v27 op_sel:[0,0,1]
	v_ashrrev_i32_e32 v27, 31, v26
	v_lshlrev_b64 v[26:27], 11, v[26:27]
	v_lshl_add_u64 v[26:27], s[10:11], 0, v[26:27]
	v_lshl_add_u64 v[26:27], v[26:27], 0, v[2:3]
	global_store_dwordx4 v[26:27], v[22:25], off sc1
	v_pk_mul_f32 v[26:27], v[72:73], v[10:11]
	v_cvt_pk_fp8_f32 v33, v140, v141 op_sel:[0,0,1]
	v_pk_mul_f32 v[22:23], v[82:83], v[20:21]
	v_pk_mul_f32 v[24:25], v[84:85], v[18:19]
	v_med3_f32 v5, v22, s63, v195
	v_med3_f32 v23, v23, s63, v195
	v_mov_b32_e32 v22, 0
	v_cvt_pk_fp8_f32 v22, v5, v23
	v_med3_f32 v5, v24, s63, v195
	v_med3_f32 v23, v25, s63, v195
	v_pk_mul_f32 v[24:25], v[74:75], v[16:17]
	v_cvt_pk_fp8_f32 v22, v5, v23 op_sel:[0,0,1]
	v_med3_f32 v5, v24, s63, v195
	v_med3_f32 v24, v25, s63, v195
	v_mov_b32_e32 v23, 0
	v_cvt_pk_fp8_f32 v23, v5, v24
	v_pk_mul_f32 v[24:25], v[76:77], v[14:15]
	global_store_dwordx4 v[200:201], v[30:33], off sc1
	v_med3_f32 v5, v24, s63, v195
	v_med3_f32 v24, v25, s63, v195
	v_cvt_pk_fp8_f32 v23, v5, v24 op_sel:[0,0,1]
	v_pk_mul_f32 v[24:25], v[70:71], v[12:13]
	s_nop 0
	v_med3_f32 v5, v24, s63, v195
	v_med3_f32 v25, v25, s63, v195
	v_mov_b32_e32 v24, 0
	v_cvt_pk_fp8_f32 v24, v5, v25
	v_med3_f32 v5, v26, s63, v195
	v_med3_f32 v25, v27, s63, v195
	v_pk_mul_f32 v[26:27], v[62:63], v[8:9]
	v_cvt_pk_fp8_f32 v24, v5, v25 op_sel:[0,0,1]
	v_med3_f32 v5, v26, s63, v195
	v_med3_f32 v26, v27, s63, v195
	v_mov_b32_e32 v25, 0
	v_cvt_pk_fp8_f32 v25, v5, v26
	v_pk_mul_f32 v[26:27], v[64:65], v[6:7]
	s_nop 0
	v_med3_f32 v5, v26, s63, v195
	v_med3_f32 v26, v27, s63, v195
	v_cvt_pk_fp8_f32 v25, v5, v26 op_sel:[0,0,1]
	v_add_u32_e32 v26, 0x90, v4
	v_ashrrev_i32_e32 v27, 31, v26
	v_lshlrev_b64 v[26:27], 11, v[26:27]
	v_lshl_add_u64 v[26:27], s[10:11], 0, v[26:27]
	v_lshl_add_u64 v[26:27], v[26:27], 0, v[2:3]
	global_store_dwordx4 v[26:27], v[22:25], off sc1
	v_pk_mul_f32 v[26:27], v[56:57], v[10:11]
	v_pk_mul_f32 v[10:11], v[40:41], v[10:11]
	v_pk_mul_f32 v[22:23], v[66:67], v[20:21]
	v_pk_mul_f32 v[24:25], v[68:69], v[18:19]
	v_med3_f32 v5, v22, s63, v195
	v_med3_f32 v23, v23, s63, v195
	v_mov_b32_e32 v22, 0
	v_cvt_pk_fp8_f32 v22, v5, v23
	v_med3_f32 v5, v24, s63, v195
	v_med3_f32 v23, v25, s63, v195
	v_pk_mul_f32 v[24:25], v[58:59], v[16:17]
	v_cvt_pk_fp8_f32 v22, v5, v23 op_sel:[0,0,1]
	v_med3_f32 v5, v24, s63, v195
	v_med3_f32 v24, v25, s63, v195
	v_mov_b32_e32 v23, 0
	v_cvt_pk_fp8_f32 v23, v5, v24
	v_pk_mul_f32 v[24:25], v[60:61], v[14:15]
	v_pk_mul_f32 v[20:21], v[50:51], v[20:21]
	v_med3_f32 v5, v24, s63, v195
	v_med3_f32 v24, v25, s63, v195
	v_cvt_pk_fp8_f32 v23, v5, v24 op_sel:[0,0,1]
	v_pk_mul_f32 v[24:25], v[54:55], v[12:13]
	v_med3_f32 v21, v21, s63, v195
	v_med3_f32 v5, v24, s63, v195
	v_med3_f32 v25, v25, s63, v195
	v_mov_b32_e32 v24, 0
	v_cvt_pk_fp8_f32 v24, v5, v25
	v_med3_f32 v5, v26, s63, v195
	v_med3_f32 v25, v27, s63, v195
	v_pk_mul_f32 v[26:27], v[46:47], v[8:9]
	v_cvt_pk_fp8_f32 v24, v5, v25 op_sel:[0,0,1]
	v_med3_f32 v5, v26, s63, v195
	v_med3_f32 v26, v27, s63, v195
	v_mov_b32_e32 v25, 0
	v_cvt_pk_fp8_f32 v25, v5, v26
	v_pk_mul_f32 v[26:27], v[48:49], v[6:7]
	v_pk_mul_f32 v[18:19], v[52:53], v[18:19]
	v_med3_f32 v5, v26, s63, v195
	v_med3_f32 v26, v27, s63, v195
	v_cvt_pk_fp8_f32 v25, v5, v26 op_sel:[0,0,1]
	v_med3_f32 v5, v20, s63, v195
	v_mov_b32_e32 v20, 0
	v_cvt_pk_fp8_f32 v20, v5, v21
	v_med3_f32 v5, v18, s63, v195
	v_med3_f32 v18, v19, s63, v195
	v_pk_mul_f32 v[16:17], v[42:43], v[16:17]
	v_add_u32_e32 v26, 0xa0, v4
	v_cvt_pk_fp8_f32 v20, v5, v18 op_sel:[0,0,1]
	v_med3_f32 v5, v16, s63, v195
	v_med3_f32 v16, v17, s63, v195
	v_mov_b32_e32 v21, 0
	v_ashrrev_i32_e32 v27, 31, v26
	v_cvt_pk_fp8_f32 v21, v5, v16
	v_lshlrev_b64 v[26:27], 11, v[26:27]
	v_lshl_add_u64 v[26:27], s[10:11], 0, v[26:27]
	v_pk_mul_f32 v[14:15], v[44:45], v[14:15]
	v_lshl_add_u64 v[26:27], v[26:27], 0, v[2:3]
	v_med3_f32 v5, v14, s63, v195
	v_med3_f32 v14, v15, s63, v195
	v_pk_mul_f32 v[12:13], v[38:39], v[12:13]
	global_store_dwordx4 v[26:27], v[22:25], off sc1
	v_cvt_pk_fp8_f32 v21, v5, v14 op_sel:[0,0,1]
	v_med3_f32 v5, v12, s63, v195
	v_med3_f32 v12, v13, s63, v195
	v_mov_b32_e32 v22, 0
	v_cvt_pk_fp8_f32 v22, v5, v12
	v_med3_f32 v5, v10, s63, v195
	v_med3_f32 v10, v11, s63, v195
	v_pk_mul_f32 v[8:9], v[34:35], v[8:9]
	v_cvt_pk_fp8_f32 v22, v5, v10 op_sel:[0,0,1]
	v_med3_f32 v5, v8, s63, v195
	v_med3_f32 v8, v9, s63, v195
	v_mov_b32_e32 v23, 0
	v_cvt_pk_fp8_f32 v23, v5, v8
	v_pk_mul_f32 v[6:7], v[36:37], v[6:7]
	v_add_u32_e32 v4, 0xb0, v4
	v_med3_f32 v5, v6, s63, v195
	v_med3_f32 v6, v7, s63, v195
	v_cvt_pk_fp8_f32 v23, v5, v6 op_sel:[0,0,1]
	v_ashrrev_i32_e32 v5, 31, v4
	v_lshlrev_b64 v[4:5], 11, v[4:5]
	v_lshl_add_u64 v[4:5], s[10:11], 0, v[4:5]
	v_lshl_add_u64 v[2:3], v[4:5], 0, v[2:3]
	global_store_dwordx4 v[2:3], v[20:23], off sc1
	s_branch .Lwtj_o
